# baseline (speedup 1.0000x reference)
_Z11pwconv_mfmaPKfPK15HIP_vector_typeIjLj4EES0_Pf:
	s_load_dwordx4 s[12:15], s[0:1], 0x0
	s_load_dwordx4 s[16:19], s[0:1], 0x10
	s_and_b32 s20, s2, 7
	s_lshr_b32 s21, s2, 3
	s_lshr_b32 s37, s20, 2
	s_and_b32 s36, s20, 3
	s_mul_i32 s36, s36, 31
	s_add_i32 s36, s36, s21
	s_lshr_b32 s21, s36, 2
	s_and_b32 s36, s36, 3
	s_lshl_b32 s37, s37, 2
	s_add_i32 s20, s37, s36
	v_lshrrev_b32_e32 v1, 6, v0
	v_and_b32_e32 v2, 63, v0
	s_nop 0
	v_readfirstlane_b32 s22, v1
	s_nop 3
	s_lshl_b32 s23, s20, 3
	s_add_i32 s23, s23, s22
	s_mul_i32 s24, s23, 0x439200
	s_mul_i32 s25, s21, 0x1f0
	s_add_u32 s24, s24, s25
	s_lshl_b32 s25, s21, 17
	s_lshl_b32 s26, s22, 13
	s_add_u32 s25, s25, s26
	s_mul_i32 s27, s20, 0x1e080
	s_mul_i32 s36, s21, 0x1f0
	s_add_u32 s27, s27, s36
	v_min_u32_e32 v10, 61, v2
	v_lshlrev_b32_e32 v3, 3, v10
	v_lshlrev_b32_e32 v4, 4, v2
	v_cmp_lt_u32_e32 vcc, 30, v10
	s_nop 1
	v_cndmask_b32_e64 v5, 0, 1, vcc
	v_mul_u32_u24_e32 v6, 31, v5
	v_sub_u32_e32 v6, v10, v6
	v_lshl_add_u32 v7, v1, 1, v5
	v_and_b32_e32 v8, 7, v6
	v_xor_b32_e32 v7, v7, v8
	v_lshlrev_b32_e32 v7, 4, v7
	v_lshl_add_u32 v5, v6, 12, v7
	s_lshl_b32 s36, s22, 2
	s_add_i32 s36, s36, 0
	s_and_b32 s36, s36, 7
	s_lshl_b32 s37, s22, 14
	s_add_i32 s37, s37, 0x0
	v_xor_b32_e32 v6, s36, v2
	v_lshlrev_b32_e32 v6, 4, v6
	v_add_u32_e32 v6, s37, v6
	s_lshl_b32 s36, s22, 2
	s_add_i32 s36, s36, 1
	s_and_b32 s36, s36, 7
	s_lshl_b32 s37, s22, 14
	s_add_i32 s37, s37, 0x1000
	v_xor_b32_e32 v7, s36, v2
	v_lshlrev_b32_e32 v7, 4, v7
	v_add_u32_e32 v7, s37, v7
	s_lshl_b32 s36, s22, 2
	s_add_i32 s36, s36, 2
	s_and_b32 s36, s36, 7
	s_lshl_b32 s37, s22, 14
	s_add_i32 s37, s37, 0x2000
	v_xor_b32_e32 v8, s36, v2
	v_lshlrev_b32_e32 v8, 4, v8
	v_add_u32_e32 v8, s37, v8
	s_lshl_b32 s36, s22, 2
	s_add_i32 s36, s36, 3
	s_and_b32 s36, s36, 7
	s_lshl_b32 s37, s22, 14
	s_add_i32 s37, s37, 0x3000
	v_xor_b32_e32 v9, s36, v2
	v_lshlrev_b32_e32 v9, 4, v9
	v_add_u32_e32 v9, s37, v9
	v_lshrrev_b32_e32 v10, 5, v0
	v_lshrrev_b32_e32 v11, 1, v10
	v_mul_u32_u24_e32 v11, 0x3c10, v11
	v_and_b32_e32 v10, 1, v10
	v_mul_u32_u24_e32 v10, 0xf8, v10
	v_add_u32_e32 v11, v11, v10
	v_and_b32_e32 v10, 31, v0
	v_lshl_add_u32 v11, v10, 3, v11
	v_add_u32_e32 v11, s27, v11
	v_cmp_eq_u32_e32 vcc, 31, v10
	v_mov_b32_e32 v10, 0x7f000000
	s_nop 1
	v_cndmask_b32_e32 v11, v11, v10, vcc
	s_waitcnt lgkmcnt(0)
	s_add_u32 s4, s12, s24
	s_addc_u32 s5, s13, 0
	s_and_b32 s5, s5, 0xffff
	s_sub_u32 s6, 0x10e48000, s24
	s_mov_b32 s7, 0x20000
	s_add_u32 s8, s14, s25
	s_addc_u32 s9, s15, 0
	s_and_b32 s9, s9, 0xffff
	s_sub_u32 s10, 0x400000, s25
	s_mov_b32 s11, 0x20000
	s_mov_b32 s28, s16
	s_and_b32 s29, s17, 0xffff
	s_mov_b32 s30, 0xf0400
	s_mov_b32 s31, 0x20000
	s_mov_b32 s32, s18
	s_and_b32 s33, s19, 0xffff
	s_mov_b32 s34, 0xf04000
	s_mov_b32 s35, 0x20000
	s_mov_b32 s40, 0x0
	s_mov_b32 s41, 0x21c90
	s_mov_b32 s42, 0x43920
	s_mov_b32 s43, 0x655b0
	s_mov_b32 s44, 0x87240
	s_mov_b32 s45, 0xa8ed0
	s_mov_b32 s46, 0xcab60
	s_mov_b32 s47, 0xec7f0
	buffer_load_dwordx2 v[44:45], v3, s[4:7], s40 offen nt
	buffer_load_dwordx2 v[46:47], v3, s[4:7], s41 offen nt
	buffer_load_dwordx2 v[48:49], v3, s[4:7], s42 offen nt
	buffer_load_dwordx2 v[50:51], v3, s[4:7], s43 offen nt
	buffer_load_dwordx2 v[52:53], v3, s[4:7], s44 offen nt
	buffer_load_dwordx2 v[54:55], v3, s[4:7], s45 offen nt
	buffer_load_dwordx2 v[56:57], v3, s[4:7], s46 offen nt
	buffer_load_dwordx2 v[58:59], v3, s[4:7], s47 offen nt
	s_mov_b32 s40, 0x10e480
	s_mov_b32 s41, 0x130110
	s_mov_b32 s42, 0x151da0
	s_mov_b32 s43, 0x173a30
	s_mov_b32 s44, 0x1956c0
	s_mov_b32 s45, 0x1b7350
	s_mov_b32 s46, 0x1d8fe0
	s_mov_b32 s47, 0x1fac70
	buffer_load_dwordx2 v[60:61], v3, s[4:7], s40 offen nt
	buffer_load_dwordx2 v[62:63], v3, s[4:7], s41 offen nt
	buffer_load_dwordx2 v[64:65], v3, s[4:7], s42 offen nt
	buffer_load_dwordx2 v[66:67], v3, s[4:7], s43 offen nt
	buffer_load_dwordx2 v[68:69], v3, s[4:7], s44 offen nt
	buffer_load_dwordx2 v[70:71], v3, s[4:7], s45 offen nt
	buffer_load_dwordx2 v[72:73], v3, s[4:7], s46 offen nt
	buffer_load_dwordx2 v[74:75], v3, s[4:7], s47 offen nt
	s_mov_b32 s40, 0x21c900
	s_mov_b32 s41, 0x23e590
	s_mov_b32 s42, 0x260220
	s_mov_b32 s43, 0x281eb0
	s_mov_b32 s44, 0x2a3b40
	s_mov_b32 s45, 0x2c57d0
	s_mov_b32 s46, 0x2e7460
	s_mov_b32 s47, 0x3090f0
	buffer_load_dwordx2 v[76:77], v3, s[4:7], s40 offen nt
	buffer_load_dwordx2 v[78:79], v3, s[4:7], s41 offen nt
	buffer_load_dwordx2 v[80:81], v3, s[4:7], s42 offen nt
	buffer_load_dwordx2 v[82:83], v3, s[4:7], s43 offen nt
	buffer_load_dwordx2 v[84:85], v3, s[4:7], s44 offen nt
	buffer_load_dwordx2 v[86:87], v3, s[4:7], s45 offen nt
	buffer_load_dwordx2 v[88:89], v3, s[4:7], s46 offen nt
	buffer_load_dwordx2 v[90:91], v3, s[4:7], s47 offen nt
	s_mov_b32 s40, 0x32ad80
	s_mov_b32 s41, 0x34ca10
	s_mov_b32 s42, 0x36e6a0
	s_mov_b32 s43, 0x390330
	s_mov_b32 s44, 0x3b1fc0
	s_mov_b32 s45, 0x3d3c50
	s_mov_b32 s46, 0x3f58e0
	s_mov_b32 s47, 0x417570
	buffer_load_dwordx2 v[92:93], v3, s[4:7], s40 offen nt
	buffer_load_dwordx2 v[94:95], v3, s[4:7], s41 offen nt
	buffer_load_dwordx2 v[96:97], v3, s[4:7], s42 offen nt
	buffer_load_dwordx2 v[98:99], v3, s[4:7], s43 offen nt
	buffer_load_dwordx2 v[100:101], v3, s[4:7], s44 offen nt
	buffer_load_dwordx2 v[102:103], v3, s[4:7], s45 offen nt
	buffer_load_dwordx2 v[104:105], v3, s[4:7], s46 offen nt
	buffer_load_dwordx2 v[106:107], v3, s[4:7], s47 offen nt
	buffer_load_dwordx2 v[252:253], v11, s[28:31], 0 offen
	s_mov_b32 s40, 0x0
	s_mov_b32 s41, 0x400
	s_mov_b32 s42, 0x800
	s_mov_b32 s43, 0xc00
	s_mov_b32 s44, 0x1000
	buffer_load_dwordx4 v[108:111], v4, s[8:11], s40 offen
	buffer_load_dwordx4 v[112:115], v4, s[8:11], s41 offen
	buffer_load_dwordx4 v[116:119], v4, s[8:11], s42 offen
	buffer_load_dwordx4 v[120:123], v4, s[8:11], s43 offen
	buffer_load_dwordx4 v[124:127], v4, s[8:11], s44 offen
	s_mov_b32 s40, 0x1400
	s_mov_b32 s41, 0x1800
	s_mov_b32 s42, 0x1c00
	s_mov_b32 s43, 0x2000
	s_mov_b32 s44, 0x2400
	buffer_load_dwordx4 v[128:131], v4, s[8:11], s40 offen
	buffer_load_dwordx4 v[132:135], v4, s[8:11], s41 offen
	buffer_load_dwordx4 v[136:139], v4, s[8:11], s42 offen
	buffer_load_dwordx4 v[140:143], v4, s[8:11], s43 offen
	buffer_load_dwordx4 v[144:147], v4, s[8:11], s44 offen
	s_mov_b32 s40, 0x10000
	s_mov_b32 s41, 0x10400
	s_mov_b32 s42, 0x10800
	s_mov_b32 s43, 0x10c00
	s_mov_b32 s44, 0x11000
	buffer_load_dwordx4 v[148:151], v4, s[8:11], s40 offen
	buffer_load_dwordx4 v[152:155], v4, s[8:11], s41 offen
	buffer_load_dwordx4 v[156:159], v4, s[8:11], s42 offen
	buffer_load_dwordx4 v[160:163], v4, s[8:11], s43 offen
	buffer_load_dwordx4 v[164:167], v4, s[8:11], s44 offen
	s_mov_b32 s40, 0x11400
	s_mov_b32 s41, 0x11800
	s_mov_b32 s42, 0x11c00
	s_mov_b32 s43, 0x12000
	s_mov_b32 s44, 0x12400
	buffer_load_dwordx4 v[168:171], v4, s[8:11], s40 offen
	buffer_load_dwordx4 v[172:175], v4, s[8:11], s41 offen
	buffer_load_dwordx4 v[176:179], v4, s[8:11], s42 offen
	buffer_load_dwordx4 v[180:183], v4, s[8:11], s43 offen
	buffer_load_dwordx4 v[184:187], v4, s[8:11], s44 offen
	s_waitcnt vmcnt(45)
	v_cvt_pkrtz_f16_f32 v12, v44, v46
	v_cvt_pkrtz_f16_f32 v13, v48, v50
	v_cvt_pkrtz_f16_f32 v14, v52, v54
	v_cvt_pkrtz_f16_f32 v15, v56, v58
	v_cvt_pkrtz_f16_f32 v16, v45, v47
	v_cvt_pkrtz_f16_f32 v17, v49, v51
	v_cvt_pkrtz_f16_f32 v18, v53, v55
	v_cvt_pkrtz_f16_f32 v19, v57, v59
	s_mov_b32 s40, 0x3c10
	s_mov_b32 s41, 0x258a0
	s_mov_b32 s42, 0x47530
	s_mov_b32 s43, 0x691c0
	s_mov_b32 s44, 0x8ae50
	s_mov_b32 s45, 0xacae0
	s_mov_b32 s46, 0xce770
	s_mov_b32 s47, 0xf0400
	buffer_load_dwordx2 v[44:45], v3, s[4:7], s40 offen nt
	buffer_load_dwordx2 v[46:47], v3, s[4:7], s41 offen nt
	buffer_load_dwordx2 v[48:49], v3, s[4:7], s42 offen nt
	buffer_load_dwordx2 v[50:51], v3, s[4:7], s43 offen nt
	buffer_load_dwordx2 v[52:53], v3, s[4:7], s44 offen nt
	buffer_load_dwordx2 v[54:55], v3, s[4:7], s45 offen nt
	buffer_load_dwordx2 v[56:57], v3, s[4:7], s46 offen nt
	buffer_load_dwordx2 v[58:59], v3, s[4:7], s47 offen nt
	ds_write_b128 v5, v[12:15] offset:0
	ds_write_b128 v5, v[16:19] offset:2048
	s_waitcnt vmcnt(45)
	v_cvt_pkrtz_f16_f32 v12, v60, v62
	v_cvt_pkrtz_f16_f32 v13, v64, v66
	v_cvt_pkrtz_f16_f32 v14, v68, v70
	v_cvt_pkrtz_f16_f32 v15, v72, v74
	v_cvt_pkrtz_f16_f32 v16, v61, v63
	v_cvt_pkrtz_f16_f32 v17, v65, v67
	v_cvt_pkrtz_f16_f32 v18, v69, v71
	v_cvt_pkrtz_f16_f32 v19, v73, v75
	s_mov_b32 s40, 0x112090
	s_mov_b32 s41, 0x133d20
	s_mov_b32 s42, 0x1559b0
	s_mov_b32 s43, 0x177640
	s_mov_b32 s44, 0x1992d0
	s_mov_b32 s45, 0x1baf60
	s_mov_b32 s46, 0x1dcbf0
	s_mov_b32 s47, 0x1fe880
	buffer_load_dwordx2 v[60:61], v3, s[4:7], s40 offen nt
	buffer_load_dwordx2 v[62:63], v3, s[4:7], s41 offen nt
	buffer_load_dwordx2 v[64:65], v3, s[4:7], s42 offen nt
	buffer_load_dwordx2 v[66:67], v3, s[4:7], s43 offen nt
	buffer_load_dwordx2 v[68:69], v3, s[4:7], s44 offen nt
	buffer_load_dwordx2 v[70:71], v3, s[4:7], s45 offen nt
	buffer_load_dwordx2 v[72:73], v3, s[4:7], s46 offen nt
	buffer_load_dwordx2 v[74:75], v3, s[4:7], s47 offen nt
	ds_write_b128 v5, v[12:15] offset:256
	ds_write_b128 v5, v[16:19] offset:2304
	s_waitcnt vmcnt(45)
	v_cvt_pkrtz_f16_f32 v12, v76, v78
	v_cvt_pkrtz_f16_f32 v13, v80, v82
	v_cvt_pkrtz_f16_f32 v14, v84, v86
	v_cvt_pkrtz_f16_f32 v15, v88, v90
	v_cvt_pkrtz_f16_f32 v16, v77, v79
	v_cvt_pkrtz_f16_f32 v17, v81, v83
	v_cvt_pkrtz_f16_f32 v18, v85, v87
	v_cvt_pkrtz_f16_f32 v19, v89, v91
	s_mov_b32 s40, 0x220510
	s_mov_b32 s41, 0x2421a0
	s_mov_b32 s42, 0x263e30
	s_mov_b32 s43, 0x285ac0
	s_mov_b32 s44, 0x2a7750
	s_mov_b32 s45, 0x2c93e0
	s_mov_b32 s46, 0x2eb070
	s_mov_b32 s47, 0x30cd00
	buffer_load_dwordx2 v[76:77], v3, s[4:7], s40 offen nt
	buffer_load_dwordx2 v[78:79], v3, s[4:7], s41 offen nt
	buffer_load_dwordx2 v[80:81], v3, s[4:7], s42 offen nt
	buffer_load_dwordx2 v[82:83], v3, s[4:7], s43 offen nt
	buffer_load_dwordx2 v[84:85], v3, s[4:7], s44 offen nt
	buffer_load_dwordx2 v[86:87], v3, s[4:7], s45 offen nt
	buffer_load_dwordx2 v[88:89], v3, s[4:7], s46 offen nt
	buffer_load_dwordx2 v[90:91], v3, s[4:7], s47 offen nt
	ds_write_b128 v5, v[12:15] offset:512
	ds_write_b128 v5, v[16:19] offset:2560
	s_waitcnt vmcnt(45)
	v_cvt_pkrtz_f16_f32 v12, v92, v94
	v_cvt_pkrtz_f16_f32 v13, v96, v98
	v_cvt_pkrtz_f16_f32 v14, v100, v102
	v_cvt_pkrtz_f16_f32 v15, v104, v106
	v_cvt_pkrtz_f16_f32 v16, v93, v95
	v_cvt_pkrtz_f16_f32 v17, v97, v99
	v_cvt_pkrtz_f16_f32 v18, v101, v103
	v_cvt_pkrtz_f16_f32 v19, v105, v107
	s_mov_b32 s40, 0x32e990
	s_mov_b32 s41, 0x350620
	s_mov_b32 s42, 0x3722b0
	s_mov_b32 s43, 0x393f40
	s_mov_b32 s44, 0x3b5bd0
	s_mov_b32 s45, 0x3d7860
	s_mov_b32 s46, 0x3f94f0
	s_mov_b32 s47, 0x41b180
	buffer_load_dwordx2 v[92:93], v3, s[4:7], s40 offen nt
	buffer_load_dwordx2 v[94:95], v3, s[4:7], s41 offen nt
	buffer_load_dwordx2 v[96:97], v3, s[4:7], s42 offen nt
	buffer_load_dwordx2 v[98:99], v3, s[4:7], s43 offen nt
	buffer_load_dwordx2 v[100:101], v3, s[4:7], s44 offen nt
	buffer_load_dwordx2 v[102:103], v3, s[4:7], s45 offen nt
	buffer_load_dwordx2 v[104:105], v3, s[4:7], s46 offen nt
	buffer_load_dwordx2 v[106:107], v3, s[4:7], s47 offen nt
	ds_write_b128 v5, v[12:15] offset:768
	ds_write_b128 v5, v[16:19] offset:2816
	s_waitcnt lgkmcnt(0)
	s_barrier
	ds_read_b128 v[12:15], v6 offset:0
	ds_read_b128 v[16:19], v6 offset:2048
	ds_read_b128 v[20:23], v7 offset:0
	ds_read_b128 v[24:27], v7 offset:2048
	ds_read_b128 v[28:31], v8 offset:0
	ds_read_b128 v[32:35], v8 offset:2048
	ds_read_b128 v[36:39], v9 offset:0
	ds_read_b128 v[40:43], v9 offset:2048
	s_waitcnt vmcnt(32)
	s_waitcnt lgkmcnt(7)
	v_mfma_f32_16x16x32_f16 v[188:191], v[108:111], v[12:15], 0
	v_mfma_f32_16x16x32_f16 v[220:223], v[148:151], v[12:15], 0
	s_waitcnt lgkmcnt(6)
	v_mfma_f32_16x16x32_f16 v[192:195], v[112:115], v[16:19], 0
	v_mfma_f32_16x16x32_f16 v[224:227], v[152:155], v[16:19], 0
	s_waitcnt lgkmcnt(5)
	v_mfma_f32_16x16x32_f16 v[196:199], v[116:119], v[20:23], 0
	v_mfma_f32_16x16x32_f16 v[228:231], v[156:159], v[20:23], 0
	s_waitcnt lgkmcnt(4)
	v_mfma_f32_16x16x32_f16 v[200:203], v[120:123], v[24:27], 0
	v_mfma_f32_16x16x32_f16 v[232:235], v[160:163], v[24:27], 0
	s_waitcnt lgkmcnt(3)
	v_mfma_f32_16x16x32_f16 v[204:207], v[124:127], v[28:31], 0
	v_mfma_f32_16x16x32_f16 v[236:239], v[164:167], v[28:31], 0
	s_waitcnt lgkmcnt(2)
	v_mfma_f32_16x16x32_f16 v[208:211], v[128:131], v[32:35], 0
	v_mfma_f32_16x16x32_f16 v[240:243], v[168:171], v[32:35], 0
	s_waitcnt lgkmcnt(1)
	v_mfma_f32_16x16x32_f16 v[212:215], v[132:135], v[36:39], 0
	v_mfma_f32_16x16x32_f16 v[244:247], v[172:175], v[36:39], 0
	s_waitcnt lgkmcnt(0)
	v_mfma_f32_16x16x32_f16 v[216:219], v[136:139], v[40:43], 0
	v_mfma_f32_16x16x32_f16 v[248:251], v[176:179], v[40:43], 0
	s_waitcnt vmcnt(24)
	v_cvt_pkrtz_f16_f32 v12, v44, v46
	v_cvt_pkrtz_f16_f32 v13, v48, v50
	v_cvt_pkrtz_f16_f32 v14, v52, v54
	v_cvt_pkrtz_f16_f32 v15, v56, v58
	v_cvt_pkrtz_f16_f32 v16, v45, v47
	v_cvt_pkrtz_f16_f32 v17, v49, v51
	v_cvt_pkrtz_f16_f32 v18, v53, v55
	v_cvt_pkrtz_f16_f32 v19, v57, v59
	s_mov_b32 s40, 0x7820
	s_mov_b32 s41, 0x294b0
	s_mov_b32 s42, 0x4b140
	s_mov_b32 s43, 0x6cdd0
	s_mov_b32 s44, 0x8ea60
	s_mov_b32 s45, 0xb06f0
	s_mov_b32 s46, 0xd2380
	s_mov_b32 s47, 0xf4010
	buffer_load_dwordx2 v[44:45], v3, s[4:7], s40 offen nt
	buffer_load_dwordx2 v[46:47], v3, s[4:7], s41 offen nt
	buffer_load_dwordx2 v[48:49], v3, s[4:7], s42 offen nt
	buffer_load_dwordx2 v[50:51], v3, s[4:7], s43 offen nt
	buffer_load_dwordx2 v[52:53], v3, s[4:7], s44 offen nt
	buffer_load_dwordx2 v[54:55], v3, s[4:7], s45 offen nt
	buffer_load_dwordx2 v[56:57], v3, s[4:7], s46 offen nt
	buffer_load_dwordx2 v[58:59], v3, s[4:7], s47 offen nt
	ds_write_b128 v5, v[12:15] offset:1024
	ds_write_b128 v5, v[16:19] offset:3072
	s_waitcnt vmcnt(24)
	v_cvt_pkrtz_f16_f32 v12, v60, v62
	v_cvt_pkrtz_f16_f32 v13, v64, v66
	v_cvt_pkrtz_f16_f32 v14, v68, v70
	v_cvt_pkrtz_f16_f32 v15, v72, v74
	v_cvt_pkrtz_f16_f32 v16, v61, v63
	v_cvt_pkrtz_f16_f32 v17, v65, v67
	v_cvt_pkrtz_f16_f32 v18, v69, v71
	v_cvt_pkrtz_f16_f32 v19, v73, v75
	s_mov_b32 s40, 0x115ca0
	s_mov_b32 s41, 0x137930
	s_mov_b32 s42, 0x1595c0
	s_mov_b32 s43, 0x17b250
	s_mov_b32 s44, 0x19cee0
	s_mov_b32 s45, 0x1beb70
	s_mov_b32 s46, 0x1e0800
	s_mov_b32 s47, 0x202490
	buffer_load_dwordx2 v[60:61], v3, s[4:7], s40 offen nt
	buffer_load_dwordx2 v[62:63], v3, s[4:7], s41 offen nt
	buffer_load_dwordx2 v[64:65], v3, s[4:7], s42 offen nt
	buffer_load_dwordx2 v[66:67], v3, s[4:7], s43 offen nt
	buffer_load_dwordx2 v[68:69], v3, s[4:7], s44 offen nt
	buffer_load_dwordx2 v[70:71], v3, s[4:7], s45 offen nt
	buffer_load_dwordx2 v[72:73], v3, s[4:7], s46 offen nt
	buffer_load_dwordx2 v[74:75], v3, s[4:7], s47 offen nt
	ds_write_b128 v5, v[12:15] offset:1280
	ds_write_b128 v5, v[16:19] offset:3328
	s_waitcnt vmcnt(24)
	v_cvt_pkrtz_f16_f32 v12, v76, v78
	v_cvt_pkrtz_f16_f32 v13, v80, v82
	v_cvt_pkrtz_f16_f32 v14, v84, v86
	v_cvt_pkrtz_f16_f32 v15, v88, v90
	v_cvt_pkrtz_f16_f32 v16, v77, v79
	v_cvt_pkrtz_f16_f32 v17, v81, v83
	v_cvt_pkrtz_f16_f32 v18, v85, v87
	v_cvt_pkrtz_f16_f32 v19, v89, v91
	s_mov_b32 s40, 0x224120
	s_mov_b32 s41, 0x245db0
	s_mov_b32 s42, 0x267a40
	s_mov_b32 s43, 0x2896d0
	s_mov_b32 s44, 0x2ab360
	s_mov_b32 s45, 0x2ccff0
	s_mov_b32 s46, 0x2eec80
	s_mov_b32 s47, 0x310910
	buffer_load_dwordx2 v[76:77], v3, s[4:7], s40 offen nt
	buffer_load_dwordx2 v[78:79], v3, s[4:7], s41 offen nt
	buffer_load_dwordx2 v[80:81], v3, s[4:7], s42 offen nt
	buffer_load_dwordx2 v[82:83], v3, s[4:7], s43 offen nt
	buffer_load_dwordx2 v[84:85], v3, s[4:7], s44 offen nt
	buffer_load_dwordx2 v[86:87], v3, s[4:7], s45 offen nt
	buffer_load_dwordx2 v[88:89], v3, s[4:7], s46 offen nt
	buffer_load_dwordx2 v[90:91], v3, s[4:7], s47 offen nt
	ds_write_b128 v5, v[12:15] offset:1536
	ds_write_b128 v5, v[16:19] offset:3584
	s_waitcnt vmcnt(24)
	v_cvt_pkrtz_f16_f32 v12, v92, v94
	v_cvt_pkrtz_f16_f32 v13, v96, v98
	v_cvt_pkrtz_f16_f32 v14, v100, v102
	v_cvt_pkrtz_f16_f32 v15, v104, v106
	v_cvt_pkrtz_f16_f32 v16, v93, v95
	v_cvt_pkrtz_f16_f32 v17, v97, v99
	v_cvt_pkrtz_f16_f32 v18, v101, v103
	v_cvt_pkrtz_f16_f32 v19, v105, v107
	s_mov_b32 s40, 0x3325a0
	s_mov_b32 s41, 0x354230
	s_mov_b32 s42, 0x375ec0
	s_mov_b32 s43, 0x397b50
	s_mov_b32 s44, 0x3b97e0
	s_mov_b32 s45, 0x3db470
	s_mov_b32 s46, 0x3fd100
	s_mov_b32 s47, 0x41ed90
	buffer_load_dwordx2 v[92:93], v3, s[4:7], s40 offen nt
	buffer_load_dwordx2 v[94:95], v3, s[4:7], s41 offen nt
	buffer_load_dwordx2 v[96:97], v3, s[4:7], s42 offen nt
	buffer_load_dwordx2 v[98:99], v3, s[4:7], s43 offen nt
	buffer_load_dwordx2 v[100:101], v3, s[4:7], s44 offen nt
	buffer_load_dwordx2 v[102:103], v3, s[4:7], s45 offen nt
	buffer_load_dwordx2 v[104:105], v3, s[4:7], s46 offen nt
	buffer_load_dwordx2 v[106:107], v3, s[4:7], s47 offen nt
	ds_write_b128 v5, v[12:15] offset:1792
	ds_write_b128 v5, v[16:19] offset:3840
	s_waitcnt lgkmcnt(0)
	s_barrier
	ds_read_b128 v[12:15], v6 offset:1024
	ds_read_b128 v[16:19], v6 offset:3072
	ds_read_b128 v[20:23], v7 offset:1024
	ds_read_b128 v[24:27], v7 offset:3072
	ds_read_b128 v[28:31], v8 offset:1024
	ds_read_b128 v[32:35], v8 offset:3072
	ds_read_b128 v[36:39], v9 offset:1024
	ds_read_b128 v[40:43], v9 offset:3072
	s_waitcnt lgkmcnt(7)
	v_mfma_f32_16x16x32_f16 v[188:191], v[112:115], v[12:15], v[188:191]
	v_mfma_f32_16x16x32_f16 v[220:223], v[152:155], v[12:15], v[220:223]
	s_waitcnt lgkmcnt(6)
	v_mfma_f32_16x16x32_f16 v[192:195], v[116:119], v[16:19], v[192:195]
	v_mfma_f32_16x16x32_f16 v[224:227], v[156:159], v[16:19], v[224:227]
	s_waitcnt lgkmcnt(5)
	v_mfma_f32_16x16x32_f16 v[196:199], v[120:123], v[20:23], v[196:199]
	v_mfma_f32_16x16x32_f16 v[228:231], v[160:163], v[20:23], v[228:231]
	s_waitcnt lgkmcnt(4)
	v_mfma_f32_16x16x32_f16 v[200:203], v[124:127], v[24:27], v[200:203]
	v_mfma_f32_16x16x32_f16 v[232:235], v[164:167], v[24:27], v[232:235]
	s_waitcnt lgkmcnt(3)
	v_mfma_f32_16x16x32_f16 v[204:207], v[128:131], v[28:31], v[204:207]
	v_mfma_f32_16x16x32_f16 v[236:239], v[168:171], v[28:31], v[236:239]
	s_waitcnt lgkmcnt(2)
	v_mfma_f32_16x16x32_f16 v[208:211], v[132:135], v[32:35], v[208:211]
	v_mfma_f32_16x16x32_f16 v[240:243], v[172:175], v[32:35], v[240:243]
	s_waitcnt lgkmcnt(1)
	v_mfma_f32_16x16x32_f16 v[212:215], v[136:139], v[36:39], v[212:215]
	v_mfma_f32_16x16x32_f16 v[244:247], v[176:179], v[36:39], v[244:247]
	s_waitcnt lgkmcnt(0)
	v_mfma_f32_16x16x32_f16 v[216:219], v[140:143], v[40:43], v[216:219]
	v_mfma_f32_16x16x32_f16 v[248:251], v[180:183], v[40:43], v[248:251]
	s_waitcnt vmcnt(24)
	v_cvt_pkrtz_f16_f32 v12, v44, v46
	v_cvt_pkrtz_f16_f32 v13, v48, v50
	v_cvt_pkrtz_f16_f32 v14, v52, v54
	v_cvt_pkrtz_f16_f32 v15, v56, v58
	v_cvt_pkrtz_f16_f32 v16, v45, v47
	v_cvt_pkrtz_f16_f32 v17, v49, v51
	v_cvt_pkrtz_f16_f32 v18, v53, v55
	v_cvt_pkrtz_f16_f32 v19, v57, v59
	s_mov_b32 s40, 0xb430
	s_mov_b32 s41, 0x2d0c0
	s_mov_b32 s42, 0x4ed50
	s_mov_b32 s43, 0x709e0
	s_mov_b32 s44, 0x92670
	s_mov_b32 s45, 0xb4300
	s_mov_b32 s46, 0xd5f90
	s_mov_b32 s47, 0xf7c20
	buffer_load_dwordx2 v[44:45], v3, s[4:7], s40 offen nt
	buffer_load_dwordx2 v[46:47], v3, s[4:7], s41 offen nt
	buffer_load_dwordx2 v[48:49], v3, s[4:7], s42 offen nt
	buffer_load_dwordx2 v[50:51], v3, s[4:7], s43 offen nt
	buffer_load_dwordx2 v[52:53], v3, s[4:7], s44 offen nt
	buffer_load_dwordx2 v[54:55], v3, s[4:7], s45 offen nt
	buffer_load_dwordx2 v[56:57], v3, s[4:7], s46 offen nt
	buffer_load_dwordx2 v[58:59], v3, s[4:7], s47 offen nt
	ds_write_b128 v5, v[12:15] offset:0
	ds_write_b128 v5, v[16:19] offset:2048
	s_waitcnt vmcnt(24)
	v_cvt_pkrtz_f16_f32 v12, v60, v62
	v_cvt_pkrtz_f16_f32 v13, v64, v66
	v_cvt_pkrtz_f16_f32 v14, v68, v70
	v_cvt_pkrtz_f16_f32 v15, v72, v74
	v_cvt_pkrtz_f16_f32 v16, v61, v63
	v_cvt_pkrtz_f16_f32 v17, v65, v67
	v_cvt_pkrtz_f16_f32 v18, v69, v71
	v_cvt_pkrtz_f16_f32 v19, v73, v75
	s_mov_b32 s40, 0x1198b0
	s_mov_b32 s41, 0x13b540
	s_mov_b32 s42, 0x15d1d0
	s_mov_b32 s43, 0x17ee60
	s_mov_b32 s44, 0x1a0af0
	s_mov_b32 s45, 0x1c2780
	s_mov_b32 s46, 0x1e4410
	s_mov_b32 s47, 0x2060a0
	buffer_load_dwordx2 v[60:61], v3, s[4:7], s40 offen nt
	buffer_load_dwordx2 v[62:63], v3, s[4:7], s41 offen nt
	buffer_load_dwordx2 v[64:65], v3, s[4:7], s42 offen nt
	buffer_load_dwordx2 v[66:67], v3, s[4:7], s43 offen nt
	buffer_load_dwordx2 v[68:69], v3, s[4:7], s44 offen nt
	buffer_load_dwordx2 v[70:71], v3, s[4:7], s45 offen nt
	buffer_load_dwordx2 v[72:73], v3, s[4:7], s46 offen nt
	buffer_load_dwordx2 v[74:75], v3, s[4:7], s47 offen nt
	ds_write_b128 v5, v[12:15] offset:256
	ds_write_b128 v5, v[16:19] offset:2304
	s_waitcnt vmcnt(24)
	v_cvt_pkrtz_f16_f32 v12, v76, v78
	v_cvt_pkrtz_f16_f32 v13, v80, v82
	v_cvt_pkrtz_f16_f32 v14, v84, v86
	v_cvt_pkrtz_f16_f32 v15, v88, v90
	v_cvt_pkrtz_f16_f32 v16, v77, v79
	v_cvt_pkrtz_f16_f32 v17, v81, v83
	v_cvt_pkrtz_f16_f32 v18, v85, v87
	v_cvt_pkrtz_f16_f32 v19, v89, v91
	s_mov_b32 s40, 0x227d30
	s_mov_b32 s41, 0x2499c0
	s_mov_b32 s42, 0x26b650
	s_mov_b32 s43, 0x28d2e0
	s_mov_b32 s44, 0x2aef70
	s_mov_b32 s45, 0x2d0c00
	s_mov_b32 s46, 0x2f2890
	s_mov_b32 s47, 0x314520
	buffer_load_dwordx2 v[76:77], v3, s[4:7], s40 offen nt
	buffer_load_dwordx2 v[78:79], v3, s[4:7], s41 offen nt
	buffer_load_dwordx2 v[80:81], v3, s[4:7], s42 offen nt
	buffer_load_dwordx2 v[82:83], v3, s[4:7], s43 offen nt
	buffer_load_dwordx2 v[84:85], v3, s[4:7], s44 offen nt
	buffer_load_dwordx2 v[86:87], v3, s[4:7], s45 offen nt
	buffer_load_dwordx2 v[88:89], v3, s[4:7], s46 offen nt
	buffer_load_dwordx2 v[90:91], v3, s[4:7], s47 offen nt
	ds_write_b128 v5, v[12:15] offset:512
	ds_write_b128 v5, v[16:19] offset:2560
	s_waitcnt vmcnt(24)
	v_cvt_pkrtz_f16_f32 v12, v92, v94
	v_cvt_pkrtz_f16_f32 v13, v96, v98
	v_cvt_pkrtz_f16_f32 v14, v100, v102
	v_cvt_pkrtz_f16_f32 v15, v104, v106
	v_cvt_pkrtz_f16_f32 v16, v93, v95
	v_cvt_pkrtz_f16_f32 v17, v97, v99
	v_cvt_pkrtz_f16_f32 v18, v101, v103
	v_cvt_pkrtz_f16_f32 v19, v105, v107
	s_mov_b32 s40, 0x3361b0
	s_mov_b32 s41, 0x357e40
	s_mov_b32 s42, 0x379ad0
	s_mov_b32 s43, 0x39b760
	s_mov_b32 s44, 0x3bd3f0
	s_mov_b32 s45, 0x3df080
	s_mov_b32 s46, 0x400d10
	s_mov_b32 s47, 0x4229a0
	buffer_load_dwordx2 v[92:93], v3, s[4:7], s40 offen nt
	buffer_load_dwordx2 v[94:95], v3, s[4:7], s41 offen nt
	buffer_load_dwordx2 v[96:97], v3, s[4:7], s42 offen nt
	buffer_load_dwordx2 v[98:99], v3, s[4:7], s43 offen nt
	buffer_load_dwordx2 v[100:101], v3, s[4:7], s44 offen nt
	buffer_load_dwordx2 v[102:103], v3, s[4:7], s45 offen nt
	buffer_load_dwordx2 v[104:105], v3, s[4:7], s46 offen nt
	buffer_load_dwordx2 v[106:107], v3, s[4:7], s47 offen nt
	ds_write_b128 v5, v[12:15] offset:768
	ds_write_b128 v5, v[16:19] offset:2816
	s_waitcnt lgkmcnt(0)
	s_barrier
	ds_read_b128 v[12:15], v6 offset:0
	ds_read_b128 v[16:19], v6 offset:2048
	ds_read_b128 v[20:23], v7 offset:0
	ds_read_b128 v[24:27], v7 offset:2048
	ds_read_b128 v[28:31], v8 offset:0
	ds_read_b128 v[32:35], v8 offset:2048
	ds_read_b128 v[36:39], v9 offset:0
	ds_read_b128 v[40:43], v9 offset:2048
	s_waitcnt lgkmcnt(7)
	v_mfma_f32_16x16x32_f16 v[188:191], v[116:119], v[12:15], v[188:191]
	v_mfma_f32_16x16x32_f16 v[220:223], v[156:159], v[12:15], v[220:223]
	s_waitcnt lgkmcnt(6)
	v_mfma_f32_16x16x32_f16 v[192:195], v[120:123], v[16:19], v[192:195]
	v_mfma_f32_16x16x32_f16 v[224:227], v[160:163], v[16:19], v[224:227]
	s_waitcnt lgkmcnt(5)
	v_mfma_f32_16x16x32_f16 v[196:199], v[124:127], v[20:23], v[196:199]
	v_mfma_f32_16x16x32_f16 v[228:231], v[164:167], v[20:23], v[228:231]
	s_waitcnt lgkmcnt(4)
	v_mfma_f32_16x16x32_f16 v[200:203], v[128:131], v[24:27], v[200:203]
	v_mfma_f32_16x16x32_f16 v[232:235], v[168:171], v[24:27], v[232:235]
	s_waitcnt lgkmcnt(3)
	v_mfma_f32_16x16x32_f16 v[204:207], v[132:135], v[28:31], v[204:207]
	v_mfma_f32_16x16x32_f16 v[236:239], v[172:175], v[28:31], v[236:239]
	s_waitcnt lgkmcnt(2)
	v_mfma_f32_16x16x32_f16 v[208:211], v[136:139], v[32:35], v[208:211]
	v_mfma_f32_16x16x32_f16 v[240:243], v[176:179], v[32:35], v[240:243]
	s_waitcnt lgkmcnt(1)
	v_mfma_f32_16x16x32_f16 v[212:215], v[140:143], v[36:39], v[212:215]
	v_mfma_f32_16x16x32_f16 v[244:247], v[180:183], v[36:39], v[244:247]
	s_waitcnt lgkmcnt(0)
	v_mfma_f32_16x16x32_f16 v[216:219], v[144:147], v[40:43], v[216:219]
	v_mfma_f32_16x16x32_f16 v[248:251], v[184:187], v[40:43], v[248:251]
	s_mov_b32 s40, 0x20000
	s_mov_b32 s41, 0x20400
	s_mov_b32 s42, 0x20800
	s_mov_b32 s43, 0x20c00
	s_mov_b32 s44, 0x21000
	buffer_load_dwordx4 v[108:111], v4, s[8:11], s40 offen
	buffer_load_dwordx4 v[112:115], v4, s[8:11], s41 offen
	buffer_load_dwordx4 v[116:119], v4, s[8:11], s42 offen
	buffer_load_dwordx4 v[120:123], v4, s[8:11], s43 offen
	buffer_load_dwordx4 v[124:127], v4, s[8:11], s44 offen
	s_mov_b32 s40, 0x21400
	s_mov_b32 s41, 0x21800
	s_mov_b32 s42, 0x21c00
	s_mov_b32 s43, 0x22000
	s_mov_b32 s44, 0x22400
	buffer_load_dwordx4 v[128:131], v4, s[8:11], s40 offen
	buffer_load_dwordx4 v[132:135], v4, s[8:11], s41 offen
	buffer_load_dwordx4 v[136:139], v4, s[8:11], s42 offen
	buffer_load_dwordx4 v[140:143], v4, s[8:11], s43 offen
	buffer_load_dwordx4 v[144:147], v4, s[8:11], s44 offen
	s_waitcnt vmcnt(34)
	v_cvt_pkrtz_f16_f32 v12, v44, v46
	v_cvt_pkrtz_f16_f32 v13, v48, v50
	v_cvt_pkrtz_f16_f32 v14, v52, v54
	v_cvt_pkrtz_f16_f32 v15, v56, v58
	v_cvt_pkrtz_f16_f32 v16, v45, v47
	v_cvt_pkrtz_f16_f32 v17, v49, v51
	v_cvt_pkrtz_f16_f32 v18, v53, v55
	v_cvt_pkrtz_f16_f32 v19, v57, v59
	s_mov_b32 s40, 0xf040
	s_mov_b32 s41, 0x30cd0
	s_mov_b32 s42, 0x52960
	s_mov_b32 s43, 0x745f0
	s_mov_b32 s44, 0x96280
	s_mov_b32 s45, 0xb7f10
	s_mov_b32 s46, 0xd9ba0
	s_mov_b32 s47, 0xfb830
	buffer_load_dwordx2 v[44:45], v3, s[4:7], s40 offen nt
	buffer_load_dwordx2 v[46:47], v3, s[4:7], s41 offen nt
	buffer_load_dwordx2 v[48:49], v3, s[4:7], s42 offen nt
	buffer_load_dwordx2 v[50:51], v3, s[4:7], s43 offen nt
	buffer_load_dwordx2 v[52:53], v3, s[4:7], s44 offen nt
	buffer_load_dwordx2 v[54:55], v3, s[4:7], s45 offen nt
	buffer_load_dwordx2 v[56:57], v3, s[4:7], s46 offen nt
	buffer_load_dwordx2 v[58:59], v3, s[4:7], s47 offen nt
	ds_write_b128 v5, v[12:15] offset:1024
	ds_write_b128 v5, v[16:19] offset:3072
	s_waitcnt vmcnt(34)
	v_cvt_pkrtz_f16_f32 v12, v60, v62
	v_cvt_pkrtz_f16_f32 v13, v64, v66
	v_cvt_pkrtz_f16_f32 v14, v68, v70
	v_cvt_pkrtz_f16_f32 v15, v72, v74
	v_cvt_pkrtz_f16_f32 v16, v61, v63
	v_cvt_pkrtz_f16_f32 v17, v65, v67
	v_cvt_pkrtz_f16_f32 v18, v69, v71
	v_cvt_pkrtz_f16_f32 v19, v73, v75
	s_mov_b32 s40, 0x11d4c0
	s_mov_b32 s41, 0x13f150
	s_mov_b32 s42, 0x160de0
	s_mov_b32 s43, 0x182a70
	s_mov_b32 s44, 0x1a4700
	s_mov_b32 s45, 0x1c6390
	s_mov_b32 s46, 0x1e8020
	s_mov_b32 s47, 0x209cb0
	buffer_load_dwordx2 v[60:61], v3, s[4:7], s40 offen nt
	buffer_load_dwordx2 v[62:63], v3, s[4:7], s41 offen nt
	buffer_load_dwordx2 v[64:65], v3, s[4:7], s42 offen nt
	buffer_load_dwordx2 v[66:67], v3, s[4:7], s43 offen nt
	buffer_load_dwordx2 v[68:69], v3, s[4:7], s44 offen nt
	buffer_load_dwordx2 v[70:71], v3, s[4:7], s45 offen nt
	buffer_load_dwordx2 v[72:73], v3, s[4:7], s46 offen nt
	buffer_load_dwordx2 v[74:75], v3, s[4:7], s47 offen nt
	ds_write_b128 v5, v[12:15] offset:1280
	ds_write_b128 v5, v[16:19] offset:3328
	s_waitcnt vmcnt(34)
	v_cvt_pkrtz_f16_f32 v12, v76, v78
	v_cvt_pkrtz_f16_f32 v13, v80, v82
	v_cvt_pkrtz_f16_f32 v14, v84, v86
	v_cvt_pkrtz_f16_f32 v15, v88, v90
	v_cvt_pkrtz_f16_f32 v16, v77, v79
	v_cvt_pkrtz_f16_f32 v17, v81, v83
	v_cvt_pkrtz_f16_f32 v18, v85, v87
	v_cvt_pkrtz_f16_f32 v19, v89, v91
	s_mov_b32 s40, 0x22b940
	s_mov_b32 s41, 0x24d5d0
	s_mov_b32 s42, 0x26f260
	s_mov_b32 s43, 0x290ef0
	s_mov_b32 s44, 0x2b2b80
	s_mov_b32 s45, 0x2d4810
	s_mov_b32 s46, 0x2f64a0
	s_mov_b32 s47, 0x318130
	buffer_load_dwordx2 v[76:77], v3, s[4:7], s40 offen nt
	buffer_load_dwordx2 v[78:79], v3, s[4:7], s41 offen nt
	buffer_load_dwordx2 v[80:81], v3, s[4:7], s42 offen nt
	buffer_load_dwordx2 v[82:83], v3, s[4:7], s43 offen nt
	buffer_load_dwordx2 v[84:85], v3, s[4:7], s44 offen nt
	buffer_load_dwordx2 v[86:87], v3, s[4:7], s45 offen nt
	buffer_load_dwordx2 v[88:89], v3, s[4:7], s46 offen nt
	buffer_load_dwordx2 v[90:91], v3, s[4:7], s47 offen nt
	ds_write_b128 v5, v[12:15] offset:1536
	ds_write_b128 v5, v[16:19] offset:3584
	s_waitcnt vmcnt(34)
	v_cvt_pkrtz_f16_f32 v12, v92, v94
	v_cvt_pkrtz_f16_f32 v13, v96, v98
	v_cvt_pkrtz_f16_f32 v14, v100, v102
	v_cvt_pkrtz_f16_f32 v15, v104, v106
	v_cvt_pkrtz_f16_f32 v16, v93, v95
	v_cvt_pkrtz_f16_f32 v17, v97, v99
	v_cvt_pkrtz_f16_f32 v18, v101, v103
	v_cvt_pkrtz_f16_f32 v19, v105, v107
	s_mov_b32 s40, 0x339dc0
	s_mov_b32 s41, 0x35ba50
	s_mov_b32 s42, 0x37d6e0
	s_mov_b32 s43, 0x39f370
	s_mov_b32 s44, 0x3c1000
	s_mov_b32 s45, 0x3e2c90
	s_mov_b32 s46, 0x404920
	s_mov_b32 s47, 0x4265b0
	buffer_load_dwordx2 v[92:93], v3, s[4:7], s40 offen nt
	buffer_load_dwordx2 v[94:95], v3, s[4:7], s41 offen nt
	buffer_load_dwordx2 v[96:97], v3, s[4:7], s42 offen nt
	buffer_load_dwordx2 v[98:99], v3, s[4:7], s43 offen nt
	buffer_load_dwordx2 v[100:101], v3, s[4:7], s44 offen nt
	buffer_load_dwordx2 v[102:103], v3, s[4:7], s45 offen nt
	buffer_load_dwordx2 v[104:105], v3, s[4:7], s46 offen nt
	buffer_load_dwordx2 v[106:107], v3, s[4:7], s47 offen nt
	ds_write_b128 v5, v[12:15] offset:1792
	ds_write_b128 v5, v[16:19] offset:3840
	s_waitcnt lgkmcnt(0)
	s_barrier
	ds_read_b128 v[12:15], v6 offset:1024
	ds_read_b128 v[16:19], v6 offset:3072
	ds_read_b128 v[20:23], v7 offset:1024
	ds_read_b128 v[24:27], v7 offset:3072
	ds_read_b128 v[28:31], v8 offset:1024
	ds_read_b128 v[32:35], v8 offset:3072
	ds_read_b128 v[36:39], v9 offset:1024
	ds_read_b128 v[40:43], v9 offset:3072
	s_waitcnt vmcnt(32)
	s_waitcnt lgkmcnt(7)
	v_mfma_f32_16x16x32_f16 v[188:191], v[148:151], v[12:15], v[188:191]
	v_mfma_f32_16x16x32_f16 v[220:223], v[108:111], v[12:15], v[220:223]
	s_waitcnt lgkmcnt(6)
	v_mfma_f32_16x16x32_f16 v[192:195], v[152:155], v[16:19], v[192:195]
	v_mfma_f32_16x16x32_f16 v[224:227], v[112:115], v[16:19], v[224:227]
	s_waitcnt lgkmcnt(5)
	v_mfma_f32_16x16x32_f16 v[196:199], v[156:159], v[20:23], v[196:199]
	v_mfma_f32_16x16x32_f16 v[228:231], v[116:119], v[20:23], v[228:231]
	s_waitcnt lgkmcnt(4)
	v_mfma_f32_16x16x32_f16 v[200:203], v[160:163], v[24:27], v[200:203]
	v_mfma_f32_16x16x32_f16 v[232:235], v[120:123], v[24:27], v[232:235]
	s_waitcnt lgkmcnt(3)
	v_mfma_f32_16x16x32_f16 v[204:207], v[164:167], v[28:31], v[204:207]
	v_mfma_f32_16x16x32_f16 v[236:239], v[124:127], v[28:31], v[236:239]
	s_waitcnt lgkmcnt(2)
	v_mfma_f32_16x16x32_f16 v[208:211], v[168:171], v[32:35], v[208:211]
	v_mfma_f32_16x16x32_f16 v[240:243], v[128:131], v[32:35], v[240:243]
	s_waitcnt lgkmcnt(1)
	v_mfma_f32_16x16x32_f16 v[212:215], v[172:175], v[36:39], v[212:215]
	v_mfma_f32_16x16x32_f16 v[244:247], v[132:135], v[36:39], v[244:247]
	s_waitcnt lgkmcnt(0)
	v_mfma_f32_16x16x32_f16 v[216:219], v[176:179], v[40:43], v[216:219]
	v_mfma_f32_16x16x32_f16 v[248:251], v[136:139], v[40:43], v[248:251]
	s_waitcnt vmcnt(24)
	v_cvt_pkrtz_f16_f32 v12, v44, v46
	v_cvt_pkrtz_f16_f32 v13, v48, v50
	v_cvt_pkrtz_f16_f32 v14, v52, v54
	v_cvt_pkrtz_f16_f32 v15, v56, v58
	v_cvt_pkrtz_f16_f32 v16, v45, v47
	v_cvt_pkrtz_f16_f32 v17, v49, v51
	v_cvt_pkrtz_f16_f32 v18, v53, v55
	v_cvt_pkrtz_f16_f32 v19, v57, v59
	s_mov_b32 s40, 0x12c50
	s_mov_b32 s41, 0x348e0
	s_mov_b32 s42, 0x56570
	s_mov_b32 s43, 0x78200
	s_mov_b32 s44, 0x99e90
	s_mov_b32 s45, 0xbbb20
	s_mov_b32 s46, 0xdd7b0
	s_mov_b32 s47, 0xff440
	buffer_load_dwordx2 v[44:45], v3, s[4:7], s40 offen nt
	buffer_load_dwordx2 v[46:47], v3, s[4:7], s41 offen nt
	buffer_load_dwordx2 v[48:49], v3, s[4:7], s42 offen nt
	buffer_load_dwordx2 v[50:51], v3, s[4:7], s43 offen nt
	buffer_load_dwordx2 v[52:53], v3, s[4:7], s44 offen nt
	buffer_load_dwordx2 v[54:55], v3, s[4:7], s45 offen nt
	buffer_load_dwordx2 v[56:57], v3, s[4:7], s46 offen nt
	buffer_load_dwordx2 v[58:59], v3, s[4:7], s47 offen nt
	ds_write_b128 v5, v[12:15] offset:0
	ds_write_b128 v5, v[16:19] offset:2048
	s_waitcnt vmcnt(24)
	v_cvt_pkrtz_f16_f32 v12, v60, v62
	v_cvt_pkrtz_f16_f32 v13, v64, v66
	v_cvt_pkrtz_f16_f32 v14, v68, v70
	v_cvt_pkrtz_f16_f32 v15, v72, v74
	v_cvt_pkrtz_f16_f32 v16, v61, v63
	v_cvt_pkrtz_f16_f32 v17, v65, v67
	v_cvt_pkrtz_f16_f32 v18, v69, v71
	v_cvt_pkrtz_f16_f32 v19, v73, v75
	s_mov_b32 s40, 0x1210d0
	s_mov_b32 s41, 0x142d60
	s_mov_b32 s42, 0x1649f0
	s_mov_b32 s43, 0x186680
	s_mov_b32 s44, 0x1a8310
	s_mov_b32 s45, 0x1c9fa0
	s_mov_b32 s46, 0x1ebc30
	s_mov_b32 s47, 0x20d8c0
	buffer_load_dwordx2 v[60:61], v3, s[4:7], s40 offen nt
	buffer_load_dwordx2 v[62:63], v3, s[4:7], s41 offen nt
	buffer_load_dwordx2 v[64:65], v3, s[4:7], s42 offen nt
	buffer_load_dwordx2 v[66:67], v3, s[4:7], s43 offen nt
	buffer_load_dwordx2 v[68:69], v3, s[4:7], s44 offen nt
	buffer_load_dwordx2 v[70:71], v3, s[4:7], s45 offen nt
	buffer_load_dwordx2 v[72:73], v3, s[4:7], s46 offen nt
	buffer_load_dwordx2 v[74:75], v3, s[4:7], s47 offen nt
	ds_write_b128 v5, v[12:15] offset:256
	ds_write_b128 v5, v[16:19] offset:2304
	s_waitcnt vmcnt(24)
	v_cvt_pkrtz_f16_f32 v12, v76, v78
	v_cvt_pkrtz_f16_f32 v13, v80, v82
	v_cvt_pkrtz_f16_f32 v14, v84, v86
	v_cvt_pkrtz_f16_f32 v15, v88, v90
	v_cvt_pkrtz_f16_f32 v16, v77, v79
	v_cvt_pkrtz_f16_f32 v17, v81, v83
	v_cvt_pkrtz_f16_f32 v18, v85, v87
	v_cvt_pkrtz_f16_f32 v19, v89, v91
	s_mov_b32 s40, 0x22f550
	s_mov_b32 s41, 0x2511e0
	s_mov_b32 s42, 0x272e70
	s_mov_b32 s43, 0x294b00
	s_mov_b32 s44, 0x2b6790
	s_mov_b32 s45, 0x2d8420
	s_mov_b32 s46, 0x2fa0b0
	s_mov_b32 s47, 0x31bd40
	buffer_load_dwordx2 v[76:77], v3, s[4:7], s40 offen nt
	buffer_load_dwordx2 v[78:79], v3, s[4:7], s41 offen nt
	buffer_load_dwordx2 v[80:81], v3, s[4:7], s42 offen nt
	buffer_load_dwordx2 v[82:83], v3, s[4:7], s43 offen nt
	buffer_load_dwordx2 v[84:85], v3, s[4:7], s44 offen nt
	buffer_load_dwordx2 v[86:87], v3, s[4:7], s45 offen nt
	buffer_load_dwordx2 v[88:89], v3, s[4:7], s46 offen nt
	buffer_load_dwordx2 v[90:91], v3, s[4:7], s47 offen nt
	ds_write_b128 v5, v[12:15] offset:512
	ds_write_b128 v5, v[16:19] offset:2560
	s_waitcnt vmcnt(24)
	v_cvt_pkrtz_f16_f32 v12, v92, v94
	v_cvt_pkrtz_f16_f32 v13, v96, v98
	v_cvt_pkrtz_f16_f32 v14, v100, v102
	v_cvt_pkrtz_f16_f32 v15, v104, v106
	v_cvt_pkrtz_f16_f32 v16, v93, v95
	v_cvt_pkrtz_f16_f32 v17, v97, v99
	v_cvt_pkrtz_f16_f32 v18, v101, v103
	v_cvt_pkrtz_f16_f32 v19, v105, v107
	s_mov_b32 s40, 0x33d9d0
	s_mov_b32 s41, 0x35f660
	s_mov_b32 s42, 0x3812f0
	s_mov_b32 s43, 0x3a2f80
	s_mov_b32 s44, 0x3c4c10
	s_mov_b32 s45, 0x3e68a0
	s_mov_b32 s46, 0x408530
	s_mov_b32 s47, 0x42a1c0
	buffer_load_dwordx2 v[92:93], v3, s[4:7], s40 offen nt
	buffer_load_dwordx2 v[94:95], v3, s[4:7], s41 offen nt
	buffer_load_dwordx2 v[96:97], v3, s[4:7], s42 offen nt
	buffer_load_dwordx2 v[98:99], v3, s[4:7], s43 offen nt
	buffer_load_dwordx2 v[100:101], v3, s[4:7], s44 offen nt
	buffer_load_dwordx2 v[102:103], v3, s[4:7], s45 offen nt
	buffer_load_dwordx2 v[104:105], v3, s[4:7], s46 offen nt
	buffer_load_dwordx2 v[106:107], v3, s[4:7], s47 offen nt
	ds_write_b128 v5, v[12:15] offset:768
	ds_write_b128 v5, v[16:19] offset:2816
	s_waitcnt lgkmcnt(0)
	s_barrier
	ds_read_b128 v[12:15], v6 offset:0
	ds_read_b128 v[16:19], v6 offset:2048
	ds_read_b128 v[20:23], v7 offset:0
	ds_read_b128 v[24:27], v7 offset:2048
	ds_read_b128 v[28:31], v8 offset:0
	ds_read_b128 v[32:35], v8 offset:2048
	ds_read_b128 v[36:39], v9 offset:0
	ds_read_b128 v[40:43], v9 offset:2048
	s_waitcnt lgkmcnt(7)
	v_mfma_f32_16x16x32_f16 v[188:191], v[152:155], v[12:15], v[188:191]
	v_mfma_f32_16x16x32_f16 v[220:223], v[112:115], v[12:15], v[220:223]
	s_waitcnt lgkmcnt(6)
	v_mfma_f32_16x16x32_f16 v[192:195], v[156:159], v[16:19], v[192:195]
	v_mfma_f32_16x16x32_f16 v[224:227], v[116:119], v[16:19], v[224:227]
	s_waitcnt lgkmcnt(5)
	v_mfma_f32_16x16x32_f16 v[196:199], v[160:163], v[20:23], v[196:199]
	v_mfma_f32_16x16x32_f16 v[228:231], v[120:123], v[20:23], v[228:231]
	s_waitcnt lgkmcnt(4)
	v_mfma_f32_16x16x32_f16 v[200:203], v[164:167], v[24:27], v[200:203]
	v_mfma_f32_16x16x32_f16 v[232:235], v[124:127], v[24:27], v[232:235]
	s_waitcnt lgkmcnt(3)
	v_mfma_f32_16x16x32_f16 v[204:207], v[168:171], v[28:31], v[204:207]
	v_mfma_f32_16x16x32_f16 v[236:239], v[128:131], v[28:31], v[236:239]
	s_waitcnt lgkmcnt(2)
	v_mfma_f32_16x16x32_f16 v[208:211], v[172:175], v[32:35], v[208:211]
	v_mfma_f32_16x16x32_f16 v[240:243], v[132:135], v[32:35], v[240:243]
	s_waitcnt lgkmcnt(1)
	v_mfma_f32_16x16x32_f16 v[212:215], v[176:179], v[36:39], v[212:215]
	v_mfma_f32_16x16x32_f16 v[244:247], v[136:139], v[36:39], v[244:247]
	s_waitcnt lgkmcnt(0)
	v_mfma_f32_16x16x32_f16 v[216:219], v[180:183], v[40:43], v[216:219]
	v_mfma_f32_16x16x32_f16 v[248:251], v[140:143], v[40:43], v[248:251]
	s_waitcnt vmcnt(24)
	v_cvt_pkrtz_f16_f32 v12, v44, v46
	v_cvt_pkrtz_f16_f32 v13, v48, v50
	v_cvt_pkrtz_f16_f32 v14, v52, v54
	v_cvt_pkrtz_f16_f32 v15, v56, v58
	v_cvt_pkrtz_f16_f32 v16, v45, v47
	v_cvt_pkrtz_f16_f32 v17, v49, v51
	v_cvt_pkrtz_f16_f32 v18, v53, v55
	v_cvt_pkrtz_f16_f32 v19, v57, v59
	s_mov_b32 s40, 0x16860
	s_mov_b32 s41, 0x384f0
	s_mov_b32 s42, 0x5a180
	s_mov_b32 s43, 0x7be10
	s_mov_b32 s44, 0x9daa0
	s_mov_b32 s45, 0xbf730
	s_mov_b32 s46, 0xe13c0
	s_mov_b32 s47, 0x103050
	buffer_load_dwordx2 v[44:45], v3, s[4:7], s40 offen nt
	buffer_load_dwordx2 v[46:47], v3, s[4:7], s41 offen nt
	buffer_load_dwordx2 v[48:49], v3, s[4:7], s42 offen nt
	buffer_load_dwordx2 v[50:51], v3, s[4:7], s43 offen nt
	buffer_load_dwordx2 v[52:53], v3, s[4:7], s44 offen nt
	buffer_load_dwordx2 v[54:55], v3, s[4:7], s45 offen nt
	buffer_load_dwordx2 v[56:57], v3, s[4:7], s46 offen nt
	buffer_load_dwordx2 v[58:59], v3, s[4:7], s47 offen nt
	ds_write_b128 v5, v[12:15] offset:1024
	ds_write_b128 v5, v[16:19] offset:3072
	s_waitcnt vmcnt(24)
	v_cvt_pkrtz_f16_f32 v12, v60, v62
	v_cvt_pkrtz_f16_f32 v13, v64, v66
	v_cvt_pkrtz_f16_f32 v14, v68, v70
	v_cvt_pkrtz_f16_f32 v15, v72, v74
	v_cvt_pkrtz_f16_f32 v16, v61, v63
	v_cvt_pkrtz_f16_f32 v17, v65, v67
	v_cvt_pkrtz_f16_f32 v18, v69, v71
	v_cvt_pkrtz_f16_f32 v19, v73, v75
	s_mov_b32 s40, 0x124ce0
	s_mov_b32 s41, 0x146970
	s_mov_b32 s42, 0x168600
	s_mov_b32 s43, 0x18a290
	s_mov_b32 s44, 0x1abf20
	s_mov_b32 s45, 0x1cdbb0
	s_mov_b32 s46, 0x1ef840
	s_mov_b32 s47, 0x2114d0
	buffer_load_dwordx2 v[60:61], v3, s[4:7], s40 offen nt
	buffer_load_dwordx2 v[62:63], v3, s[4:7], s41 offen nt
	buffer_load_dwordx2 v[64:65], v3, s[4:7], s42 offen nt
	buffer_load_dwordx2 v[66:67], v3, s[4:7], s43 offen nt
	buffer_load_dwordx2 v[68:69], v3, s[4:7], s44 offen nt
	buffer_load_dwordx2 v[70:71], v3, s[4:7], s45 offen nt
	buffer_load_dwordx2 v[72:73], v3, s[4:7], s46 offen nt
	buffer_load_dwordx2 v[74:75], v3, s[4:7], s47 offen nt
	ds_write_b128 v5, v[12:15] offset:1280
	ds_write_b128 v5, v[16:19] offset:3328
	s_waitcnt vmcnt(24)
	v_cvt_pkrtz_f16_f32 v12, v76, v78
	v_cvt_pkrtz_f16_f32 v13, v80, v82
	v_cvt_pkrtz_f16_f32 v14, v84, v86
	v_cvt_pkrtz_f16_f32 v15, v88, v90
	v_cvt_pkrtz_f16_f32 v16, v77, v79
	v_cvt_pkrtz_f16_f32 v17, v81, v83
	v_cvt_pkrtz_f16_f32 v18, v85, v87
	v_cvt_pkrtz_f16_f32 v19, v89, v91
	s_mov_b32 s40, 0x233160
	s_mov_b32 s41, 0x254df0
	s_mov_b32 s42, 0x276a80
	s_mov_b32 s43, 0x298710
	s_mov_b32 s44, 0x2ba3a0
	s_mov_b32 s45, 0x2dc030
	s_mov_b32 s46, 0x2fdcc0
	s_mov_b32 s47, 0x31f950
	buffer_load_dwordx2 v[76:77], v3, s[4:7], s40 offen nt
	buffer_load_dwordx2 v[78:79], v3, s[4:7], s41 offen nt
	buffer_load_dwordx2 v[80:81], v3, s[4:7], s42 offen nt
	buffer_load_dwordx2 v[82:83], v3, s[4:7], s43 offen nt
	buffer_load_dwordx2 v[84:85], v3, s[4:7], s44 offen nt
	buffer_load_dwordx2 v[86:87], v3, s[4:7], s45 offen nt
	buffer_load_dwordx2 v[88:89], v3, s[4:7], s46 offen nt
	buffer_load_dwordx2 v[90:91], v3, s[4:7], s47 offen nt
	ds_write_b128 v5, v[12:15] offset:1536
	ds_write_b128 v5, v[16:19] offset:3584
	s_waitcnt vmcnt(24)
	v_cvt_pkrtz_f16_f32 v12, v92, v94
	v_cvt_pkrtz_f16_f32 v13, v96, v98
	v_cvt_pkrtz_f16_f32 v14, v100, v102
	v_cvt_pkrtz_f16_f32 v15, v104, v106
	v_cvt_pkrtz_f16_f32 v16, v93, v95
	v_cvt_pkrtz_f16_f32 v17, v97, v99
	v_cvt_pkrtz_f16_f32 v18, v101, v103
	v_cvt_pkrtz_f16_f32 v19, v105, v107
	s_mov_b32 s40, 0x3415e0
	s_mov_b32 s41, 0x363270
	s_mov_b32 s42, 0x384f00
	s_mov_b32 s43, 0x3a6b90
	s_mov_b32 s44, 0x3c8820
	s_mov_b32 s45, 0x3ea4b0
	s_mov_b32 s46, 0x40c140
	s_mov_b32 s47, 0x42ddd0
	buffer_load_dwordx2 v[92:93], v3, s[4:7], s40 offen nt
	buffer_load_dwordx2 v[94:95], v3, s[4:7], s41 offen nt
	buffer_load_dwordx2 v[96:97], v3, s[4:7], s42 offen nt
	buffer_load_dwordx2 v[98:99], v3, s[4:7], s43 offen nt
	buffer_load_dwordx2 v[100:101], v3, s[4:7], s44 offen nt
	buffer_load_dwordx2 v[102:103], v3, s[4:7], s45 offen nt
	buffer_load_dwordx2 v[104:105], v3, s[4:7], s46 offen nt
	buffer_load_dwordx2 v[106:107], v3, s[4:7], s47 offen nt
	ds_write_b128 v5, v[12:15] offset:1792
	ds_write_b128 v5, v[16:19] offset:3840
	s_waitcnt lgkmcnt(0)
	s_barrier
	ds_read_b128 v[12:15], v6 offset:1024
	ds_read_b128 v[16:19], v6 offset:3072
	ds_read_b128 v[20:23], v7 offset:1024
	ds_read_b128 v[24:27], v7 offset:3072
	ds_read_b128 v[28:31], v8 offset:1024
	ds_read_b128 v[32:35], v8 offset:3072
	ds_read_b128 v[36:39], v9 offset:1024
	ds_read_b128 v[40:43], v9 offset:3072
	s_waitcnt lgkmcnt(7)
	v_mfma_f32_16x16x32_f16 v[188:191], v[156:159], v[12:15], v[188:191]
	v_mfma_f32_16x16x32_f16 v[220:223], v[116:119], v[12:15], v[220:223]
	s_waitcnt lgkmcnt(6)
	v_mfma_f32_16x16x32_f16 v[192:195], v[160:163], v[16:19], v[192:195]
	v_mfma_f32_16x16x32_f16 v[224:227], v[120:123], v[16:19], v[224:227]
	s_waitcnt lgkmcnt(5)
	v_mfma_f32_16x16x32_f16 v[196:199], v[164:167], v[20:23], v[196:199]
	v_mfma_f32_16x16x32_f16 v[228:231], v[124:127], v[20:23], v[228:231]
	s_waitcnt lgkmcnt(4)
	v_mfma_f32_16x16x32_f16 v[200:203], v[168:171], v[24:27], v[200:203]
	v_mfma_f32_16x16x32_f16 v[232:235], v[128:131], v[24:27], v[232:235]
	s_waitcnt lgkmcnt(3)
	v_mfma_f32_16x16x32_f16 v[204:207], v[172:175], v[28:31], v[204:207]
	v_mfma_f32_16x16x32_f16 v[236:239], v[132:135], v[28:31], v[236:239]
	s_waitcnt lgkmcnt(2)
	v_mfma_f32_16x16x32_f16 v[208:211], v[176:179], v[32:35], v[208:211]
	v_mfma_f32_16x16x32_f16 v[240:243], v[136:139], v[32:35], v[240:243]
	s_waitcnt lgkmcnt(1)
	v_mfma_f32_16x16x32_f16 v[212:215], v[180:183], v[36:39], v[212:215]
	v_mfma_f32_16x16x32_f16 v[244:247], v[140:143], v[36:39], v[244:247]
	s_waitcnt lgkmcnt(0)
	v_mfma_f32_16x16x32_f16 v[216:219], v[184:187], v[40:43], v[216:219]
	v_mfma_f32_16x16x32_f16 v[248:251], v[144:147], v[40:43], v[248:251]
	s_mov_b32 s40, 0x30000
	s_mov_b32 s41, 0x30400
	s_mov_b32 s42, 0x30800
	s_mov_b32 s43, 0x30c00
	s_mov_b32 s44, 0x31000
	buffer_load_dwordx4 v[148:151], v4, s[8:11], s40 offen
	buffer_load_dwordx4 v[152:155], v4, s[8:11], s41 offen
	buffer_load_dwordx4 v[156:159], v4, s[8:11], s42 offen
	buffer_load_dwordx4 v[160:163], v4, s[8:11], s43 offen
	buffer_load_dwordx4 v[164:167], v4, s[8:11], s44 offen
	s_mov_b32 s40, 0x31400
	s_mov_b32 s41, 0x31800
	s_mov_b32 s42, 0x31c00
	s_mov_b32 s43, 0x32000
	s_mov_b32 s44, 0x32400
	buffer_load_dwordx4 v[168:171], v4, s[8:11], s40 offen
	buffer_load_dwordx4 v[172:175], v4, s[8:11], s41 offen
	buffer_load_dwordx4 v[176:179], v4, s[8:11], s42 offen
	buffer_load_dwordx4 v[180:183], v4, s[8:11], s43 offen
	buffer_load_dwordx4 v[184:187], v4, s[8:11], s44 offen
	s_waitcnt vmcnt(34)
	v_cvt_pkrtz_f16_f32 v12, v44, v46
	v_cvt_pkrtz_f16_f32 v13, v48, v50
	v_cvt_pkrtz_f16_f32 v14, v52, v54
	v_cvt_pkrtz_f16_f32 v15, v56, v58
	v_cvt_pkrtz_f16_f32 v16, v45, v47
	v_cvt_pkrtz_f16_f32 v17, v49, v51
	v_cvt_pkrtz_f16_f32 v18, v53, v55
	v_cvt_pkrtz_f16_f32 v19, v57, v59
	s_mov_b32 s40, 0x1a470
	s_mov_b32 s41, 0x3c100
	s_mov_b32 s42, 0x5dd90
	s_mov_b32 s43, 0x7fa20
	s_mov_b32 s44, 0xa16b0
	s_mov_b32 s45, 0xc3340
	s_mov_b32 s46, 0xe4fd0
	s_mov_b32 s47, 0x106c60
	buffer_load_dwordx2 v[44:45], v3, s[4:7], s40 offen nt
	buffer_load_dwordx2 v[46:47], v3, s[4:7], s41 offen nt
	buffer_load_dwordx2 v[48:49], v3, s[4:7], s42 offen nt
	buffer_load_dwordx2 v[50:51], v3, s[4:7], s43 offen nt
	buffer_load_dwordx2 v[52:53], v3, s[4:7], s44 offen nt
	buffer_load_dwordx2 v[54:55], v3, s[4:7], s45 offen nt
	buffer_load_dwordx2 v[56:57], v3, s[4:7], s46 offen nt
	buffer_load_dwordx2 v[58:59], v3, s[4:7], s47 offen nt
	ds_write_b128 v5, v[12:15] offset:0
	ds_write_b128 v5, v[16:19] offset:2048
	s_waitcnt vmcnt(34)
	v_cvt_pkrtz_f16_f32 v12, v60, v62
	v_cvt_pkrtz_f16_f32 v13, v64, v66
	v_cvt_pkrtz_f16_f32 v14, v68, v70
	v_cvt_pkrtz_f16_f32 v15, v72, v74
	v_cvt_pkrtz_f16_f32 v16, v61, v63
	v_cvt_pkrtz_f16_f32 v17, v65, v67
	v_cvt_pkrtz_f16_f32 v18, v69, v71
	v_cvt_pkrtz_f16_f32 v19, v73, v75
	s_mov_b32 s40, 0x1288f0
	s_mov_b32 s41, 0x14a580
	s_mov_b32 s42, 0x16c210
	s_mov_b32 s43, 0x18dea0
	s_mov_b32 s44, 0x1afb30
	s_mov_b32 s45, 0x1d17c0
	s_mov_b32 s46, 0x1f3450
	s_mov_b32 s47, 0x2150e0
	buffer_load_dwordx2 v[60:61], v3, s[4:7], s40 offen nt
	buffer_load_dwordx2 v[62:63], v3, s[4:7], s41 offen nt
	buffer_load_dwordx2 v[64:65], v3, s[4:7], s42 offen nt
	buffer_load_dwordx2 v[66:67], v3, s[4:7], s43 offen nt
	buffer_load_dwordx2 v[68:69], v3, s[4:7], s44 offen nt
	buffer_load_dwordx2 v[70:71], v3, s[4:7], s45 offen nt
	buffer_load_dwordx2 v[72:73], v3, s[4:7], s46 offen nt
	buffer_load_dwordx2 v[74:75], v3, s[4:7], s47 offen nt
	ds_write_b128 v5, v[12:15] offset:256
	ds_write_b128 v5, v[16:19] offset:2304
	s_waitcnt vmcnt(34)
	v_cvt_pkrtz_f16_f32 v12, v76, v78
	v_cvt_pkrtz_f16_f32 v13, v80, v82
	v_cvt_pkrtz_f16_f32 v14, v84, v86
	v_cvt_pkrtz_f16_f32 v15, v88, v90
	v_cvt_pkrtz_f16_f32 v16, v77, v79
	v_cvt_pkrtz_f16_f32 v17, v81, v83
	v_cvt_pkrtz_f16_f32 v18, v85, v87
	v_cvt_pkrtz_f16_f32 v19, v89, v91
	s_mov_b32 s40, 0x236d70
	s_mov_b32 s41, 0x258a00
	s_mov_b32 s42, 0x27a690
	s_mov_b32 s43, 0x29c320
	s_mov_b32 s44, 0x2bdfb0
	s_mov_b32 s45, 0x2dfc40
	s_mov_b32 s46, 0x3018d0
	s_mov_b32 s47, 0x323560
	buffer_load_dwordx2 v[76:77], v3, s[4:7], s40 offen nt
	buffer_load_dwordx2 v[78:79], v3, s[4:7], s41 offen nt
	buffer_load_dwordx2 v[80:81], v3, s[4:7], s42 offen nt
	buffer_load_dwordx2 v[82:83], v3, s[4:7], s43 offen nt
	buffer_load_dwordx2 v[84:85], v3, s[4:7], s44 offen nt
	buffer_load_dwordx2 v[86:87], v3, s[4:7], s45 offen nt
	buffer_load_dwordx2 v[88:89], v3, s[4:7], s46 offen nt
	buffer_load_dwordx2 v[90:91], v3, s[4:7], s47 offen nt
	ds_write_b128 v5, v[12:15] offset:512
	ds_write_b128 v5, v[16:19] offset:2560
	s_waitcnt vmcnt(34)
	v_cvt_pkrtz_f16_f32 v12, v92, v94
	v_cvt_pkrtz_f16_f32 v13, v96, v98
	v_cvt_pkrtz_f16_f32 v14, v100, v102
	v_cvt_pkrtz_f16_f32 v15, v104, v106
	v_cvt_pkrtz_f16_f32 v16, v93, v95
	v_cvt_pkrtz_f16_f32 v17, v97, v99
	v_cvt_pkrtz_f16_f32 v18, v101, v103
	v_cvt_pkrtz_f16_f32 v19, v105, v107
	s_mov_b32 s40, 0x3451f0
	s_mov_b32 s41, 0x366e80
	s_mov_b32 s42, 0x388b10
	s_mov_b32 s43, 0x3aa7a0
	s_mov_b32 s44, 0x3cc430
	s_mov_b32 s45, 0x3ee0c0
	s_mov_b32 s46, 0x40fd50
	s_mov_b32 s47, 0x4319e0
	buffer_load_dwordx2 v[92:93], v3, s[4:7], s40 offen nt
	buffer_load_dwordx2 v[94:95], v3, s[4:7], s41 offen nt
	buffer_load_dwordx2 v[96:97], v3, s[4:7], s42 offen nt
	buffer_load_dwordx2 v[98:99], v3, s[4:7], s43 offen nt
	buffer_load_dwordx2 v[100:101], v3, s[4:7], s44 offen nt
	buffer_load_dwordx2 v[102:103], v3, s[4:7], s45 offen nt
	buffer_load_dwordx2 v[104:105], v3, s[4:7], s46 offen nt
	buffer_load_dwordx2 v[106:107], v3, s[4:7], s47 offen nt
	ds_write_b128 v5, v[12:15] offset:768
	ds_write_b128 v5, v[16:19] offset:2816
	s_waitcnt lgkmcnt(0)
	s_barrier
	ds_read_b128 v[12:15], v6 offset:0
	ds_read_b128 v[16:19], v6 offset:2048
	ds_read_b128 v[20:23], v7 offset:0
	ds_read_b128 v[24:27], v7 offset:2048
	ds_read_b128 v[28:31], v8 offset:0
	ds_read_b128 v[32:35], v8 offset:2048
	ds_read_b128 v[36:39], v9 offset:0
	ds_read_b128 v[40:43], v9 offset:2048
	s_waitcnt vmcnt(32)
	s_waitcnt lgkmcnt(7)
	v_mfma_f32_16x16x32_f16 v[188:191], v[108:111], v[12:15], v[188:191]
	v_mfma_f32_16x16x32_f16 v[220:223], v[148:151], v[12:15], v[220:223]
	s_waitcnt lgkmcnt(6)
	v_mfma_f32_16x16x32_f16 v[192:195], v[112:115], v[16:19], v[192:195]
	v_mfma_f32_16x16x32_f16 v[224:227], v[152:155], v[16:19], v[224:227]
	s_waitcnt lgkmcnt(5)
	v_mfma_f32_16x16x32_f16 v[196:199], v[116:119], v[20:23], v[196:199]
	v_mfma_f32_16x16x32_f16 v[228:231], v[156:159], v[20:23], v[228:231]
	s_waitcnt lgkmcnt(4)
	v_mfma_f32_16x16x32_f16 v[200:203], v[120:123], v[24:27], v[200:203]
	v_mfma_f32_16x16x32_f16 v[232:235], v[160:163], v[24:27], v[232:235]
	s_waitcnt lgkmcnt(3)
	v_mfma_f32_16x16x32_f16 v[204:207], v[124:127], v[28:31], v[204:207]
	v_mfma_f32_16x16x32_f16 v[236:239], v[164:167], v[28:31], v[236:239]
	s_waitcnt lgkmcnt(2)
	v_mfma_f32_16x16x32_f16 v[208:211], v[128:131], v[32:35], v[208:211]
	v_mfma_f32_16x16x32_f16 v[240:243], v[168:171], v[32:35], v[240:243]
	s_waitcnt lgkmcnt(1)
	v_mfma_f32_16x16x32_f16 v[212:215], v[132:135], v[36:39], v[212:215]
	v_mfma_f32_16x16x32_f16 v[244:247], v[172:175], v[36:39], v[244:247]
	s_waitcnt lgkmcnt(0)
	v_mfma_f32_16x16x32_f16 v[216:219], v[136:139], v[40:43], v[216:219]
	v_mfma_f32_16x16x32_f16 v[248:251], v[176:179], v[40:43], v[248:251]
	s_waitcnt vmcnt(24)
	v_cvt_pkrtz_f16_f32 v12, v44, v46
	v_cvt_pkrtz_f16_f32 v13, v48, v50
	v_cvt_pkrtz_f16_f32 v14, v52, v54
	v_cvt_pkrtz_f16_f32 v15, v56, v58
	v_cvt_pkrtz_f16_f32 v16, v45, v47
	v_cvt_pkrtz_f16_f32 v17, v49, v51
	v_cvt_pkrtz_f16_f32 v18, v53, v55
	v_cvt_pkrtz_f16_f32 v19, v57, v59
	s_mov_b32 s40, 0x1e080
	s_mov_b32 s41, 0x3fd10
	s_mov_b32 s42, 0x619a0
	s_mov_b32 s43, 0x83630
	s_mov_b32 s44, 0xa52c0
	s_mov_b32 s45, 0xc6f50
	s_mov_b32 s46, 0xe8be0
	s_mov_b32 s47, 0x10a870
	buffer_load_dwordx2 v[44:45], v3, s[4:7], s40 offen nt
	buffer_load_dwordx2 v[46:47], v3, s[4:7], s41 offen nt
	buffer_load_dwordx2 v[48:49], v3, s[4:7], s42 offen nt
	buffer_load_dwordx2 v[50:51], v3, s[4:7], s43 offen nt
	buffer_load_dwordx2 v[52:53], v3, s[4:7], s44 offen nt
	buffer_load_dwordx2 v[54:55], v3, s[4:7], s45 offen nt
	buffer_load_dwordx2 v[56:57], v3, s[4:7], s46 offen nt
	buffer_load_dwordx2 v[58:59], v3, s[4:7], s47 offen nt
	ds_write_b128 v5, v[12:15] offset:1024
	ds_write_b128 v5, v[16:19] offset:3072
	s_waitcnt vmcnt(24)
	v_cvt_pkrtz_f16_f32 v12, v60, v62
	v_cvt_pkrtz_f16_f32 v13, v64, v66
	v_cvt_pkrtz_f16_f32 v14, v68, v70
	v_cvt_pkrtz_f16_f32 v15, v72, v74
	v_cvt_pkrtz_f16_f32 v16, v61, v63
	v_cvt_pkrtz_f16_f32 v17, v65, v67
	v_cvt_pkrtz_f16_f32 v18, v69, v71
	v_cvt_pkrtz_f16_f32 v19, v73, v75
	s_mov_b32 s40, 0x12c500
	s_mov_b32 s41, 0x14e190
	s_mov_b32 s42, 0x16fe20
	s_mov_b32 s43, 0x191ab0
	s_mov_b32 s44, 0x1b3740
	s_mov_b32 s45, 0x1d53d0
	s_mov_b32 s46, 0x1f7060
	s_mov_b32 s47, 0x218cf0
	buffer_load_dwordx2 v[60:61], v3, s[4:7], s40 offen nt
	buffer_load_dwordx2 v[62:63], v3, s[4:7], s41 offen nt
	buffer_load_dwordx2 v[64:65], v3, s[4:7], s42 offen nt
	buffer_load_dwordx2 v[66:67], v3, s[4:7], s43 offen nt
	buffer_load_dwordx2 v[68:69], v3, s[4:7], s44 offen nt
	buffer_load_dwordx2 v[70:71], v3, s[4:7], s45 offen nt
	buffer_load_dwordx2 v[72:73], v3, s[4:7], s46 offen nt
	buffer_load_dwordx2 v[74:75], v3, s[4:7], s47 offen nt
	ds_write_b128 v5, v[12:15] offset:1280
	ds_write_b128 v5, v[16:19] offset:3328
	s_waitcnt vmcnt(24)
	v_cvt_pkrtz_f16_f32 v12, v76, v78
	v_cvt_pkrtz_f16_f32 v13, v80, v82
	v_cvt_pkrtz_f16_f32 v14, v84, v86
	v_cvt_pkrtz_f16_f32 v15, v88, v90
	v_cvt_pkrtz_f16_f32 v16, v77, v79
	v_cvt_pkrtz_f16_f32 v17, v81, v83
	v_cvt_pkrtz_f16_f32 v18, v85, v87
	v_cvt_pkrtz_f16_f32 v19, v89, v91
	s_mov_b32 s40, 0x23a980
	s_mov_b32 s41, 0x25c610
	s_mov_b32 s42, 0x27e2a0
	s_mov_b32 s43, 0x29ff30
	s_mov_b32 s44, 0x2c1bc0
	s_mov_b32 s45, 0x2e3850
	s_mov_b32 s46, 0x3054e0
	s_mov_b32 s47, 0x327170
	buffer_load_dwordx2 v[76:77], v3, s[4:7], s40 offen nt
	buffer_load_dwordx2 v[78:79], v3, s[4:7], s41 offen nt
	buffer_load_dwordx2 v[80:81], v3, s[4:7], s42 offen nt
	buffer_load_dwordx2 v[82:83], v3, s[4:7], s43 offen nt
	buffer_load_dwordx2 v[84:85], v3, s[4:7], s44 offen nt
	buffer_load_dwordx2 v[86:87], v3, s[4:7], s45 offen nt
	buffer_load_dwordx2 v[88:89], v3, s[4:7], s46 offen nt
	buffer_load_dwordx2 v[90:91], v3, s[4:7], s47 offen nt
	ds_write_b128 v5, v[12:15] offset:1536
	ds_write_b128 v5, v[16:19] offset:3584
	s_waitcnt vmcnt(24)
	v_cvt_pkrtz_f16_f32 v12, v92, v94
	v_cvt_pkrtz_f16_f32 v13, v96, v98
	v_cvt_pkrtz_f16_f32 v14, v100, v102
	v_cvt_pkrtz_f16_f32 v15, v104, v106
	v_cvt_pkrtz_f16_f32 v16, v93, v95
	v_cvt_pkrtz_f16_f32 v17, v97, v99
	v_cvt_pkrtz_f16_f32 v18, v101, v103
	v_cvt_pkrtz_f16_f32 v19, v105, v107
	s_mov_b32 s40, 0x348e00
	s_mov_b32 s41, 0x36aa90
	s_mov_b32 s42, 0x38c720
	s_mov_b32 s43, 0x3ae3b0
	s_mov_b32 s44, 0x3d0040
	s_mov_b32 s45, 0x3f1cd0
	s_mov_b32 s46, 0x413960
	s_mov_b32 s47, 0x4355f0
	buffer_load_dwordx2 v[92:93], v3, s[4:7], s40 offen nt
	buffer_load_dwordx2 v[94:95], v3, s[4:7], s41 offen nt
	buffer_load_dwordx2 v[96:97], v3, s[4:7], s42 offen nt
	buffer_load_dwordx2 v[98:99], v3, s[4:7], s43 offen nt
	buffer_load_dwordx2 v[100:101], v3, s[4:7], s44 offen nt
	buffer_load_dwordx2 v[102:103], v3, s[4:7], s45 offen nt
	buffer_load_dwordx2 v[104:105], v3, s[4:7], s46 offen nt
	buffer_load_dwordx2 v[106:107], v3, s[4:7], s47 offen nt
	ds_write_b128 v5, v[12:15] offset:1792
	ds_write_b128 v5, v[16:19] offset:3840
	s_waitcnt lgkmcnt(0)
	s_barrier
	ds_read_b128 v[12:15], v6 offset:1024
	ds_read_b128 v[16:19], v6 offset:3072
	ds_read_b128 v[20:23], v7 offset:1024
	ds_read_b128 v[24:27], v7 offset:3072
	ds_read_b128 v[28:31], v8 offset:1024
	ds_read_b128 v[32:35], v8 offset:3072
	ds_read_b128 v[36:39], v9 offset:1024
	ds_read_b128 v[40:43], v9 offset:3072
	s_waitcnt lgkmcnt(7)
	v_mfma_f32_16x16x32_f16 v[188:191], v[112:115], v[12:15], v[188:191]
	v_mfma_f32_16x16x32_f16 v[220:223], v[152:155], v[12:15], v[220:223]
	s_waitcnt lgkmcnt(6)
	v_mfma_f32_16x16x32_f16 v[192:195], v[116:119], v[16:19], v[192:195]
	v_mfma_f32_16x16x32_f16 v[224:227], v[156:159], v[16:19], v[224:227]
	s_waitcnt lgkmcnt(5)
	v_mfma_f32_16x16x32_f16 v[196:199], v[120:123], v[20:23], v[196:199]
	v_mfma_f32_16x16x32_f16 v[228:231], v[160:163], v[20:23], v[228:231]
	s_waitcnt lgkmcnt(4)
	v_mfma_f32_16x16x32_f16 v[200:203], v[124:127], v[24:27], v[200:203]
	v_mfma_f32_16x16x32_f16 v[232:235], v[164:167], v[24:27], v[232:235]
	s_waitcnt lgkmcnt(3)
	v_mfma_f32_16x16x32_f16 v[204:207], v[128:131], v[28:31], v[204:207]
	v_mfma_f32_16x16x32_f16 v[236:239], v[168:171], v[28:31], v[236:239]
	s_waitcnt lgkmcnt(2)
	v_mfma_f32_16x16x32_f16 v[208:211], v[132:135], v[32:35], v[208:211]
	v_mfma_f32_16x16x32_f16 v[240:243], v[172:175], v[32:35], v[240:243]
	s_waitcnt lgkmcnt(1)
	v_mfma_f32_16x16x32_f16 v[212:215], v[136:139], v[36:39], v[212:215]
	v_mfma_f32_16x16x32_f16 v[244:247], v[176:179], v[36:39], v[244:247]
	s_waitcnt lgkmcnt(0)
	v_mfma_f32_16x16x32_f16 v[216:219], v[140:143], v[40:43], v[216:219]
	v_mfma_f32_16x16x32_f16 v[248:251], v[180:183], v[40:43], v[248:251]
	s_waitcnt vmcnt(24)
	v_cvt_pkrtz_f16_f32 v12, v44, v46
	v_cvt_pkrtz_f16_f32 v13, v48, v50
	v_cvt_pkrtz_f16_f32 v14, v52, v54
	v_cvt_pkrtz_f16_f32 v15, v56, v58
	v_cvt_pkrtz_f16_f32 v16, v45, v47
	v_cvt_pkrtz_f16_f32 v17, v49, v51
	v_cvt_pkrtz_f16_f32 v18, v53, v55
	v_cvt_pkrtz_f16_f32 v19, v57, v59
	ds_write_b128 v5, v[12:15] offset:0
	ds_write_b128 v5, v[16:19] offset:2048
	s_waitcnt vmcnt(16)
	v_cvt_pkrtz_f16_f32 v12, v60, v62
	v_cvt_pkrtz_f16_f32 v13, v64, v66
	v_cvt_pkrtz_f16_f32 v14, v68, v70
	v_cvt_pkrtz_f16_f32 v15, v72, v74
	v_cvt_pkrtz_f16_f32 v16, v61, v63
	v_cvt_pkrtz_f16_f32 v17, v65, v67
	v_cvt_pkrtz_f16_f32 v18, v69, v71
	v_cvt_pkrtz_f16_f32 v19, v73, v75
	ds_write_b128 v5, v[12:15] offset:256
	ds_write_b128 v5, v[16:19] offset:2304
	s_waitcnt vmcnt(8)
	v_cvt_pkrtz_f16_f32 v12, v76, v78
	v_cvt_pkrtz_f16_f32 v13, v80, v82
	v_cvt_pkrtz_f16_f32 v14, v84, v86
	v_cvt_pkrtz_f16_f32 v15, v88, v90
	v_cvt_pkrtz_f16_f32 v16, v77, v79
	v_cvt_pkrtz_f16_f32 v17, v81, v83
	v_cvt_pkrtz_f16_f32 v18, v85, v87
	v_cvt_pkrtz_f16_f32 v19, v89, v91
	ds_write_b128 v5, v[12:15] offset:512
	ds_write_b128 v5, v[16:19] offset:2560
	s_waitcnt vmcnt(0)
	v_cvt_pkrtz_f16_f32 v12, v92, v94
	v_cvt_pkrtz_f16_f32 v13, v96, v98
	v_cvt_pkrtz_f16_f32 v14, v100, v102
	v_cvt_pkrtz_f16_f32 v15, v104, v106
	v_cvt_pkrtz_f16_f32 v16, v93, v95
	v_cvt_pkrtz_f16_f32 v17, v97, v99
	v_cvt_pkrtz_f16_f32 v18, v101, v103
	v_cvt_pkrtz_f16_f32 v19, v105, v107
	ds_write_b128 v5, v[12:15] offset:768
	ds_write_b128 v5, v[16:19] offset:2816
	s_waitcnt lgkmcnt(0)
	s_barrier
	ds_read_b128 v[12:15], v6 offset:0
	ds_read_b128 v[16:19], v6 offset:2048
	ds_read_b128 v[20:23], v7 offset:0
	ds_read_b128 v[24:27], v7 offset:2048
	ds_read_b128 v[28:31], v8 offset:0
	ds_read_b128 v[32:35], v8 offset:2048
	ds_read_b128 v[36:39], v9 offset:0
	ds_read_b128 v[40:43], v9 offset:2048
	s_waitcnt lgkmcnt(7)
	v_mfma_f32_16x16x32_f16 v[188:191], v[116:119], v[12:15], v[188:191]
	v_mfma_f32_16x16x32_f16 v[220:223], v[156:159], v[12:15], v[220:223]
	s_waitcnt lgkmcnt(6)
	v_mfma_f32_16x16x32_f16 v[192:195], v[120:123], v[16:19], v[192:195]
	v_mfma_f32_16x16x32_f16 v[224:227], v[160:163], v[16:19], v[224:227]
	s_waitcnt lgkmcnt(5)
	v_mfma_f32_16x16x32_f16 v[196:199], v[124:127], v[20:23], v[196:199]
	v_mfma_f32_16x16x32_f16 v[228:231], v[164:167], v[20:23], v[228:231]
	s_waitcnt lgkmcnt(4)
	v_mfma_f32_16x16x32_f16 v[200:203], v[128:131], v[24:27], v[200:203]
	v_mfma_f32_16x16x32_f16 v[232:235], v[168:171], v[24:27], v[232:235]
	s_waitcnt lgkmcnt(3)
	v_mfma_f32_16x16x32_f16 v[204:207], v[132:135], v[28:31], v[204:207]
	v_mfma_f32_16x16x32_f16 v[236:239], v[172:175], v[28:31], v[236:239]
	s_waitcnt lgkmcnt(2)
	v_mfma_f32_16x16x32_f16 v[208:211], v[136:139], v[32:35], v[208:211]
	v_mfma_f32_16x16x32_f16 v[240:243], v[176:179], v[32:35], v[240:243]
	s_waitcnt lgkmcnt(1)
	v_mfma_f32_16x16x32_f16 v[212:215], v[140:143], v[36:39], v[212:215]
	v_mfma_f32_16x16x32_f16 v[244:247], v[180:183], v[36:39], v[244:247]
	s_waitcnt lgkmcnt(0)
	v_mfma_f32_16x16x32_f16 v[216:219], v[144:147], v[40:43], v[216:219]
	v_mfma_f32_16x16x32_f16 v[248:251], v[184:187], v[40:43], v[248:251]
	s_nop 7
	s_nop 3
	v_and_b32_e32 v10, 1, v0
	v_cmp_eq_u32_e32 vcc, 1, v10
	s_nop 1
	v_cndmask_b32_e32 v188, v188, v220, vcc
	v_cndmask_b32_e32 v189, v189, v221, vcc
	v_cndmask_b32_e32 v190, v190, v222, vcc
	v_cndmask_b32_e32 v191, v191, v223, vcc
	v_cndmask_b32_e32 v192, v192, v224, vcc
	v_cndmask_b32_e32 v193, v193, v225, vcc
	v_cndmask_b32_e32 v194, v194, v226, vcc
	v_cndmask_b32_e32 v195, v195, v227, vcc
	v_cndmask_b32_e32 v196, v196, v228, vcc
	v_cndmask_b32_e32 v197, v197, v229, vcc
	v_cndmask_b32_e32 v198, v198, v230, vcc
	v_cndmask_b32_e32 v199, v199, v231, vcc
	v_cndmask_b32_e32 v200, v200, v232, vcc
	v_cndmask_b32_e32 v201, v201, v233, vcc
	v_cndmask_b32_e32 v202, v202, v234, vcc
	v_cndmask_b32_e32 v203, v203, v235, vcc
	v_cndmask_b32_e32 v204, v204, v236, vcc
	v_cndmask_b32_e32 v205, v205, v237, vcc
	v_cndmask_b32_e32 v206, v206, v238, vcc
	v_cndmask_b32_e32 v207, v207, v239, vcc
	v_cndmask_b32_e32 v208, v208, v240, vcc
	v_cndmask_b32_e32 v209, v209, v241, vcc
	v_cndmask_b32_e32 v210, v210, v242, vcc
	v_cndmask_b32_e32 v211, v211, v243, vcc
	v_cndmask_b32_e32 v212, v212, v244, vcc
	v_cndmask_b32_e32 v213, v213, v245, vcc
	v_cndmask_b32_e32 v214, v214, v246, vcc
	v_cndmask_b32_e32 v215, v215, v247, vcc
	v_cndmask_b32_e32 v216, v216, v248, vcc
	v_cndmask_b32_e32 v217, v217, v249, vcc
	v_cndmask_b32_e32 v218, v218, v250, vcc
	v_cndmask_b32_e32 v219, v219, v251, vcc
	s_barrier
	v_lshrrev_b32_e32 v10, 4, v2
	v_lshlrev_b32_e32 v10, 6, v10
	v_and_b32_e32 v12, 15, v2
	v_add_u32_e32 v10, v10, v12
	v_mul_u32_u24_e32 v10, 0x108, v10
	v_lshl_add_u32 v10, v1, 5, v10
	ds_write_b32 v10, v188 offset:0
	ds_write_b32 v10, v189 offset:4224
	ds_write_b32 v10, v190 offset:8448
	ds_write_b32 v10, v191 offset:12672
	ds_write_b32 v10, v192 offset:4
	ds_write_b32 v10, v193 offset:4228
	ds_write_b32 v10, v194 offset:8452
	ds_write_b32 v10, v195 offset:12676
	s_waitcnt lgkmcnt(4)
	ds_write_b32 v10, v196 offset:8
	ds_write_b32 v10, v197 offset:4232
	ds_write_b32 v10, v198 offset:8456
	ds_write_b32 v10, v199 offset:12680
	ds_write_b32 v10, v200 offset:12
	ds_write_b32 v10, v201 offset:4236
	ds_write_b32 v10, v202 offset:8460
	ds_write_b32 v10, v203 offset:12684
	s_waitcnt lgkmcnt(4)
	ds_write_b32 v10, v204 offset:16
	ds_write_b32 v10, v205 offset:4240
	ds_write_b32 v10, v206 offset:8464
	ds_write_b32 v10, v207 offset:12688
	ds_write_b32 v10, v208 offset:20
	ds_write_b32 v10, v209 offset:4244
	ds_write_b32 v10, v210 offset:8468
	ds_write_b32 v10, v211 offset:12692
	s_waitcnt lgkmcnt(4)
	ds_write_b32 v10, v212 offset:24
	ds_write_b32 v10, v213 offset:4248
	ds_write_b32 v10, v214 offset:8472
	ds_write_b32 v10, v215 offset:12696
	ds_write_b32 v10, v216 offset:28
	ds_write_b32 v10, v217 offset:4252
	ds_write_b32 v10, v218 offset:8476
	ds_write_b32 v10, v219 offset:12700
	s_waitcnt lgkmcnt(0)
	s_barrier
	v_lshrrev_b32_e32 v12, 5, v0
	v_mul_u32_u24_e32 v12, 0x108, v12
	v_and_b32_e32 v13, 31, v0
	v_lshl_add_u32 v12, v13, 3, v12
	ds_read_b64 v[44:45], v12 offset:0
	ds_read_b64 v[46:47], v12 offset:4224
	ds_read_b64 v[48:49], v12 offset:8448
	ds_read_b64 v[50:51], v12 offset:12672
	ds_read_b64 v[52:53], v12 offset:16896
	ds_read_b64 v[54:55], v12 offset:21120
	ds_read_b64 v[56:57], v12 offset:25344
	ds_read_b64 v[58:59], v12 offset:29568
	s_waitcnt lgkmcnt(7)
	v_add_f32_e32 v44, v252, v44
	v_add_f32_e32 v45, v253, v45
	s_mov_b32 s40, 0x0
	buffer_store_dwordx2 v[44:45], v11, s[32:35], s40 offen nt
	s_waitcnt lgkmcnt(6)
	v_add_f32_e32 v46, v252, v46
	v_add_f32_e32 v47, v253, v47
	s_mov_b32 s41, 0xf0400
	buffer_store_dwordx2 v[46:47], v11, s[32:35], s41 offen nt
	s_waitcnt lgkmcnt(5)
	v_add_f32_e32 v48, v252, v48
	v_add_f32_e32 v49, v253, v49
	s_mov_b32 s42, 0x1e0800
	buffer_store_dwordx2 v[48:49], v11, s[32:35], s42 offen nt
	s_waitcnt lgkmcnt(4)
	v_add_f32_e32 v50, v252, v50
	v_add_f32_e32 v51, v253, v51
	s_mov_b32 s43, 0x2d0c00
	buffer_store_dwordx2 v[50:51], v11, s[32:35], s43 offen nt
	s_waitcnt lgkmcnt(3)
	v_add_f32_e32 v52, v252, v52
	v_add_f32_e32 v53, v253, v53
	s_mov_b32 s44, 0x3c1000
	buffer_store_dwordx2 v[52:53], v11, s[32:35], s44 offen nt
	s_waitcnt lgkmcnt(2)
	v_add_f32_e32 v54, v252, v54
	v_add_f32_e32 v55, v253, v55
	s_mov_b32 s45, 0x4b1400
	buffer_store_dwordx2 v[54:55], v11, s[32:35], s45 offen nt
	s_waitcnt lgkmcnt(1)
	v_add_f32_e32 v56, v252, v56
	v_add_f32_e32 v57, v253, v57
	s_mov_b32 s46, 0x5a1800
	buffer_store_dwordx2 v[56:57], v11, s[32:35], s46 offen nt
	s_waitcnt lgkmcnt(0)
	v_add_f32_e32 v58, v252, v58
	v_add_f32_e32 v59, v253, v59
	s_mov_b32 s47, 0x691c00
	buffer_store_dwordx2 v[58:59], v11, s[32:35], s47 offen nt
	ds_read_b64 v[60:61], v12 offset:33792
	ds_read_b64 v[62:63], v12 offset:38016
	ds_read_b64 v[64:65], v12 offset:42240
	ds_read_b64 v[66:67], v12 offset:46464
	ds_read_b64 v[68:69], v12 offset:50688
	ds_read_b64 v[70:71], v12 offset:54912
	ds_read_b64 v[72:73], v12 offset:59136
	ds_read_b64 v[74:75], v12 offset:63360
	s_waitcnt lgkmcnt(7)
	v_add_f32_e32 v60, v252, v60
	v_add_f32_e32 v61, v253, v61
	s_mov_b32 s40, 0x782000
	buffer_store_dwordx2 v[60:61], v11, s[32:35], s40 offen nt
	s_waitcnt lgkmcnt(6)
	v_add_f32_e32 v62, v252, v62
	v_add_f32_e32 v63, v253, v63
	s_mov_b32 s41, 0x872400
	buffer_store_dwordx2 v[62:63], v11, s[32:35], s41 offen nt
	s_waitcnt lgkmcnt(5)
	v_add_f32_e32 v64, v252, v64
	v_add_f32_e32 v65, v253, v65
	s_mov_b32 s42, 0x962800
	buffer_store_dwordx2 v[64:65], v11, s[32:35], s42 offen nt
	s_waitcnt lgkmcnt(4)
	v_add_f32_e32 v66, v252, v66
	v_add_f32_e32 v67, v253, v67
	s_mov_b32 s43, 0xa52c00
	buffer_store_dwordx2 v[66:67], v11, s[32:35], s43 offen nt
	s_waitcnt lgkmcnt(3)
	v_add_f32_e32 v68, v252, v68
	v_add_f32_e32 v69, v253, v69
	s_mov_b32 s44, 0xb43000
	buffer_store_dwordx2 v[68:69], v11, s[32:35], s44 offen nt
	s_waitcnt lgkmcnt(2)
	v_add_f32_e32 v70, v252, v70
	v_add_f32_e32 v71, v253, v71
	s_mov_b32 s45, 0xc33400
	buffer_store_dwordx2 v[70:71], v11, s[32:35], s45 offen nt
	s_waitcnt lgkmcnt(1)
	v_add_f32_e32 v72, v252, v72
	v_add_f32_e32 v73, v253, v73
	s_mov_b32 s46, 0xd23800
	buffer_store_dwordx2 v[72:73], v11, s[32:35], s46 offen nt
	s_waitcnt lgkmcnt(0)
	v_add_f32_e32 v74, v252, v74
	v_add_f32_e32 v75, v253, v75
	s_mov_b32 s47, 0xe13c00
	buffer_store_dwordx2 v[74:75], v11, s[32:35], s47 offen nt
	s_endpgm
